# bf16 GEMM loops (in-proj u/kv, mix, out-proj): priority toggles around the MFMA clusters removed, on top of v144
# baseline (speedup 1.0000x reference)
.Lpeel170:
	ds_read_b128 v[142:145], v136
	ds_read_b128 v[146:149], v136 offset:1024
	ds_read_b128 v[150:153], v136 offset:2048
	ds_read_b128 v[154:157], v136 offset:3072
	ds_read_b128 v[158:161], v137
	ds_read_b128 v[162:165], v137 offset:1024
	ds_read_b128 v[166:169], v137 offset:2048
	ds_read_b128 v[174:177], v137 offset:3072
	s_add_u32 s14, s12, 0x100
	s_addc_u32 s15, s13, 0
	s_cmp_eq_u32 s56, 12
	s_cselect_b32 s20, s10, s14
	s_cselect_b32 s21, s11, s15
	s_cselect_b32 s18, s8, s54
	s_cselect_b32 s19, s9, s55
	s_add_u32 s16, s20, 0x80
	s_addc_u32 s17, s21, 0
	ds_read_b128 v[178:181], v138
	ds_read_b128 v[182:185], v138 offset:1024
	ds_read_b128 v[186:189], v138 offset:2048
	ds_read_b128 v[190:193], v138 offset:3072
	ds_read_b128 v[194:197], v138 offset:4096
	ds_read_b128 v[198:201], v138 offset:5120
	ds_read_b128 v[202:205], v138 offset:6144
	ds_read_b128 v[206:209], v138 offset:7168
	s_add_u32 s12, s12, 0x40080
	s_addc_u32 s13, s13, 0
	s_mov_b32 s57, m0
	s_mov_b32 m0, s52
	s_nop 2
	global_load_lds_dwordx4 v132, s[12:13]
	s_mov_b32 m0, s57
	s_nop 0
	s_mov_b32 s57, m0
	s_mov_b32 m0, s53
	s_nop 2
	global_load_lds_dwordx4 v134, s[12:13]
	s_mov_b32 m0, s57
	s_waitcnt vmcnt(8)
	s_waitcnt lgkmcnt(0)
	s_barrier
	v_mfma_f32_16x16x32_bf16 v[126:129], v[142:145], v[178:181], 0
	v_mfma_f32_16x16x32_bf16 v[122:125], v[150:153], v[178:181], 0
	v_mfma_f32_16x16x32_bf16 v[110:113], v[142:145], v[186:189], 0
	v_mfma_f32_16x16x32_bf16 v[106:109], v[150:153], v[186:189], 0
	v_mfma_f32_16x16x32_bf16 v[94:97], v[142:145], v[194:197], 0
	v_mfma_f32_16x16x32_bf16 v[90:93], v[150:153], v[194:197], 0
	v_mfma_f32_16x16x32_bf16 v[78:81], v[142:145], v[202:205], 0
	v_mfma_f32_16x16x32_bf16 v[74:77], v[150:153], v[202:205], 0
	v_mfma_f32_16x16x32_bf16 v[126:129], v[146:149], v[182:185], v[126:129]
	v_mfma_f32_16x16x32_bf16 v[122:125], v[154:157], v[182:185], v[122:125]
	v_mfma_f32_16x16x32_bf16 v[110:113], v[146:149], v[190:193], v[110:113]
	v_mfma_f32_16x16x32_bf16 v[106:109], v[154:157], v[190:193], v[106:109]
	v_mfma_f32_16x16x32_bf16 v[94:97], v[146:149], v[198:201], v[94:97]
	v_mfma_f32_16x16x32_bf16 v[90:93], v[154:157], v[198:201], v[90:93]
	v_mfma_f32_16x16x32_bf16 v[78:81], v[146:149], v[206:209], v[78:81]
	v_mfma_f32_16x16x32_bf16 v[74:77], v[154:157], v[206:209], v[74:77]
	v_mfma_f32_16x16x32_bf16 v[118:121], v[158:161], v[178:181], 0
	v_mfma_f32_16x16x32_bf16 v[114:117], v[166:169], v[178:181], 0
	v_mfma_f32_16x16x32_bf16 v[102:105], v[158:161], v[186:189], 0
	v_mfma_f32_16x16x32_bf16 v[98:101], v[166:169], v[186:189], 0
	v_mfma_f32_16x16x32_bf16 v[86:89], v[158:161], v[194:197], 0
	v_mfma_f32_16x16x32_bf16 v[82:85], v[166:169], v[194:197], 0
	v_mfma_f32_16x16x32_bf16 v[70:73], v[158:161], v[202:205], 0
	v_mfma_f32_16x16x32_bf16 v[66:69], v[166:169], v[202:205], 0
	v_mfma_f32_16x16x32_bf16 v[118:121], v[162:165], v[182:185], v[118:121]
	v_mfma_f32_16x16x32_bf16 v[114:117], v[174:177], v[182:185], v[114:117]
	v_mfma_f32_16x16x32_bf16 v[102:105], v[162:165], v[190:193], v[102:105]
	v_mfma_f32_16x16x32_bf16 v[98:101], v[174:177], v[190:193], v[98:101]
	v_mfma_f32_16x16x32_bf16 v[86:89], v[162:165], v[198:201], v[86:89]
	v_mfma_f32_16x16x32_bf16 v[82:85], v[174:177], v[198:201], v[82:85]
	v_mfma_f32_16x16x32_bf16 v[70:73], v[162:165], v[206:209], v[70:73]
	v_mfma_f32_16x16x32_bf16 v[66:69], v[174:177], v[206:209], v[66:69]
	s_barrier
	ds_read_b128 v[178:181], v138 offset:16384
	ds_read_b128 v[182:185], v138 offset:17408
	ds_read_b128 v[186:189], v138 offset:18432
	ds_read_b128 v[190:193], v138 offset:19456
	ds_read_b128 v[194:197], v138 offset:20480
	ds_read_b128 v[198:201], v138 offset:21504
	ds_read_b128 v[202:205], v138 offset:22528
	ds_read_b128 v[206:209], v138 offset:23552
	s_mov_b32 s12, m0
	s_mov_b32 m0, s24
	s_nop 2
	global_load_lds_dwordx4 v133, s[18:19]
	s_mov_b32 m0, s12
	s_nop 0
	s_mov_b32 s12, m0
	s_mov_b32 m0, s25
	s_nop 2
	global_load_lds_dwordx4 v135, s[18:19]
	s_mov_b32 m0, s12
	s_add_u32 s12, s18, 0x40000
	s_addc_u32 s13, s19, 0
	s_mov_b32 s57, m0
	s_mov_b32 m0, s28
	s_nop 2
	global_load_lds_dwordx4 v133, s[12:13]
	s_mov_b32 m0, s57
	s_nop 0
	s_mov_b32 s57, m0
	s_mov_b32 m0, s29
	s_nop 2
	global_load_lds_dwordx4 v135, s[12:13]
	s_mov_b32 m0, s57
	s_mov_b32 s12, m0
	s_mov_b32 m0, s5
	s_nop 2
	global_load_lds_dwordx4 v132, s[20:21]
	s_mov_b32 m0, s12
	s_nop 0
	s_mov_b32 s12, m0
	s_mov_b32 m0, s30
	s_nop 2
	global_load_lds_dwordx4 v134, s[20:21]
	s_mov_b32 m0, s12
	s_waitcnt vmcnt(8)
	s_waitcnt lgkmcnt(0)
	s_barrier
	v_mfma_f32_16x16x32_bf16 v[62:65], v[142:145], v[178:181], 0
	v_mfma_f32_16x16x32_bf16 v[58:61], v[150:153], v[178:181], 0
	v_mfma_f32_16x16x32_bf16 v[46:49], v[142:145], v[186:189], 0
	v_mfma_f32_16x16x32_bf16 v[42:45], v[150:153], v[186:189], 0
	v_mfma_f32_16x16x32_bf16 v[30:33], v[142:145], v[194:197], 0
	v_mfma_f32_16x16x32_bf16 v[26:29], v[150:153], v[194:197], 0
	v_mfma_f32_16x16x32_bf16 v[14:17], v[142:145], v[202:205], 0
	v_mfma_f32_16x16x32_bf16 v[10:13], v[150:153], v[202:205], 0
	v_mfma_f32_16x16x32_bf16 v[62:65], v[146:149], v[182:185], v[62:65]
	v_mfma_f32_16x16x32_bf16 v[58:61], v[154:157], v[182:185], v[58:61]
	v_mfma_f32_16x16x32_bf16 v[46:49], v[146:149], v[190:193], v[46:49]
	v_mfma_f32_16x16x32_bf16 v[42:45], v[154:157], v[190:193], v[42:45]
	v_mfma_f32_16x16x32_bf16 v[30:33], v[146:149], v[198:201], v[30:33]
	v_mfma_f32_16x16x32_bf16 v[26:29], v[154:157], v[198:201], v[26:29]
	v_mfma_f32_16x16x32_bf16 v[14:17], v[146:149], v[206:209], v[14:17]
	v_mfma_f32_16x16x32_bf16 v[10:13], v[154:157], v[206:209], v[10:13]
	v_mfma_f32_16x16x32_bf16 v[54:57], v[158:161], v[178:181], 0
	v_mfma_f32_16x16x32_bf16 v[50:53], v[166:169], v[178:181], 0
	v_mfma_f32_16x16x32_bf16 v[38:41], v[158:161], v[186:189], 0
	v_mfma_f32_16x16x32_bf16 v[34:37], v[166:169], v[186:189], 0
	v_mfma_f32_16x16x32_bf16 v[22:25], v[158:161], v[194:197], 0
	v_mfma_f32_16x16x32_bf16 v[18:21], v[166:169], v[194:197], 0
	v_mfma_f32_16x16x32_bf16 v[6:9], v[158:161], v[202:205], 0
	v_mfma_f32_16x16x32_bf16 v[2:5], v[166:169], v[202:205], 0
	v_mfma_f32_16x16x32_bf16 v[54:57], v[162:165], v[182:185], v[54:57]
	v_mfma_f32_16x16x32_bf16 v[50:53], v[174:177], v[182:185], v[50:53]
	v_mfma_f32_16x16x32_bf16 v[38:41], v[162:165], v[190:193], v[38:41]
	v_mfma_f32_16x16x32_bf16 v[34:37], v[174:177], v[190:193], v[34:37]
	v_mfma_f32_16x16x32_bf16 v[22:25], v[162:165], v[198:201], v[22:25]
	v_mfma_f32_16x16x32_bf16 v[18:21], v[174:177], v[198:201], v[18:21]
	v_mfma_f32_16x16x32_bf16 v[6:9], v[162:165], v[206:209], v[6:9]
	v_mfma_f32_16x16x32_bf16 v[2:5], v[174:177], v[206:209], v[2:5]
	s_barrier
	s_branch .Lmid170
.LBB0_170:
	ds_read_b128 v[142:145], v136
	ds_read_b128 v[146:149], v136 offset:1024
	ds_read_b128 v[150:153], v136 offset:2048
	ds_read_b128 v[154:157], v136 offset:3072
	ds_read_b128 v[158:161], v137
	ds_read_b128 v[162:165], v137 offset:1024
	ds_read_b128 v[166:169], v137 offset:2048
	ds_read_b128 v[174:177], v137 offset:3072
	s_add_u32 s14, s12, 0x100
	s_addc_u32 s15, s13, 0
	s_cmp_eq_u32 s56, 12
	s_cselect_b32 s20, s10, s14
	s_cselect_b32 s21, s11, s15
	s_cselect_b32 s18, s8, s54
	s_cselect_b32 s19, s9, s55
	s_add_u32 s16, s20, 0x80
	s_addc_u32 s17, s21, 0
	ds_read_b128 v[178:181], v138
	ds_read_b128 v[182:185], v138 offset:1024
	ds_read_b128 v[186:189], v138 offset:2048
	ds_read_b128 v[190:193], v138 offset:3072
	ds_read_b128 v[194:197], v138 offset:4096
	ds_read_b128 v[198:201], v138 offset:5120
	ds_read_b128 v[202:205], v138 offset:6144
	ds_read_b128 v[206:209], v138 offset:7168
	s_add_u32 s12, s12, 0x40080
	s_addc_u32 s13, s13, 0
	s_mov_b32 s57, m0
	s_mov_b32 m0, s52
	s_nop 2
	global_load_lds_dwordx4 v132, s[12:13]
	s_mov_b32 m0, s57
	s_nop 0
	s_mov_b32 s57, m0
	s_mov_b32 m0, s53
	s_nop 2
	global_load_lds_dwordx4 v134, s[12:13]
	s_mov_b32 m0, s57
	s_waitcnt vmcnt(8)
	s_waitcnt lgkmcnt(0)
	s_barrier
	v_mfma_f32_16x16x32_bf16 v[126:129], v[142:145], v[178:181], v[126:129]
	v_mfma_f32_16x16x32_bf16 v[122:125], v[150:153], v[178:181], v[122:125]
	v_mfma_f32_16x16x32_bf16 v[110:113], v[142:145], v[186:189], v[110:113]
	v_mfma_f32_16x16x32_bf16 v[106:109], v[150:153], v[186:189], v[106:109]
	v_mfma_f32_16x16x32_bf16 v[94:97], v[142:145], v[194:197], v[94:97]
	v_mfma_f32_16x16x32_bf16 v[90:93], v[150:153], v[194:197], v[90:93]
	v_mfma_f32_16x16x32_bf16 v[78:81], v[142:145], v[202:205], v[78:81]
	v_mfma_f32_16x16x32_bf16 v[74:77], v[150:153], v[202:205], v[74:77]
	v_mfma_f32_16x16x32_bf16 v[126:129], v[146:149], v[182:185], v[126:129]
	v_mfma_f32_16x16x32_bf16 v[122:125], v[154:157], v[182:185], v[122:125]
	v_mfma_f32_16x16x32_bf16 v[110:113], v[146:149], v[190:193], v[110:113]
	v_mfma_f32_16x16x32_bf16 v[106:109], v[154:157], v[190:193], v[106:109]
	v_mfma_f32_16x16x32_bf16 v[94:97], v[146:149], v[198:201], v[94:97]
	v_mfma_f32_16x16x32_bf16 v[90:93], v[154:157], v[198:201], v[90:93]
	v_mfma_f32_16x16x32_bf16 v[78:81], v[146:149], v[206:209], v[78:81]
	v_mfma_f32_16x16x32_bf16 v[74:77], v[154:157], v[206:209], v[74:77]
	v_mfma_f32_16x16x32_bf16 v[118:121], v[158:161], v[178:181], v[118:121]
	v_mfma_f32_16x16x32_bf16 v[114:117], v[166:169], v[178:181], v[114:117]
	v_mfma_f32_16x16x32_bf16 v[102:105], v[158:161], v[186:189], v[102:105]
	v_mfma_f32_16x16x32_bf16 v[98:101], v[166:169], v[186:189], v[98:101]
	v_mfma_f32_16x16x32_bf16 v[86:89], v[158:161], v[194:197], v[86:89]
	v_mfma_f32_16x16x32_bf16 v[82:85], v[166:169], v[194:197], v[82:85]
	v_mfma_f32_16x16x32_bf16 v[70:73], v[158:161], v[202:205], v[70:73]
	v_mfma_f32_16x16x32_bf16 v[66:69], v[166:169], v[202:205], v[66:69]
	v_mfma_f32_16x16x32_bf16 v[118:121], v[162:165], v[182:185], v[118:121]
	v_mfma_f32_16x16x32_bf16 v[114:117], v[174:177], v[182:185], v[114:117]
	v_mfma_f32_16x16x32_bf16 v[102:105], v[162:165], v[190:193], v[102:105]
	v_mfma_f32_16x16x32_bf16 v[98:101], v[174:177], v[190:193], v[98:101]
	v_mfma_f32_16x16x32_bf16 v[86:89], v[162:165], v[198:201], v[86:89]
	v_mfma_f32_16x16x32_bf16 v[82:85], v[174:177], v[198:201], v[82:85]
	v_mfma_f32_16x16x32_bf16 v[70:73], v[162:165], v[206:209], v[70:73]
	v_mfma_f32_16x16x32_bf16 v[66:69], v[174:177], v[206:209], v[66:69]
	s_barrier
	ds_read_b128 v[178:181], v138 offset:16384
	ds_read_b128 v[182:185], v138 offset:17408
	ds_read_b128 v[186:189], v138 offset:18432
	ds_read_b128 v[190:193], v138 offset:19456
	ds_read_b128 v[194:197], v138 offset:20480
	ds_read_b128 v[198:201], v138 offset:21504
	ds_read_b128 v[202:205], v138 offset:22528
	ds_read_b128 v[206:209], v138 offset:23552
	s_mov_b32 s12, m0
	s_mov_b32 m0, s24
	s_nop 2
	global_load_lds_dwordx4 v133, s[18:19]
	s_mov_b32 m0, s12
	s_nop 0
	s_mov_b32 s12, m0
	s_mov_b32 m0, s25
	s_nop 2
	global_load_lds_dwordx4 v135, s[18:19]
	s_mov_b32 m0, s12
	s_add_u32 s12, s18, 0x40000
	s_addc_u32 s13, s19, 0
	s_mov_b32 s57, m0
	s_mov_b32 m0, s28
	s_nop 2
	global_load_lds_dwordx4 v133, s[12:13]
	s_mov_b32 m0, s57
	s_nop 0
	s_mov_b32 s57, m0
	s_mov_b32 m0, s29
	s_nop 2
	global_load_lds_dwordx4 v135, s[12:13]
	s_mov_b32 m0, s57
	s_mov_b32 s12, m0
	s_mov_b32 m0, s5
	s_nop 2
	global_load_lds_dwordx4 v132, s[20:21]
	s_mov_b32 m0, s12
	s_nop 0
	s_mov_b32 s12, m0
	s_mov_b32 m0, s30
	s_nop 2
	global_load_lds_dwordx4 v134, s[20:21]
	s_mov_b32 m0, s12
	s_waitcnt vmcnt(8)
	s_waitcnt lgkmcnt(0)
	s_barrier
	v_mfma_f32_16x16x32_bf16 v[62:65], v[142:145], v[178:181], v[62:65]
	v_mfma_f32_16x16x32_bf16 v[58:61], v[150:153], v[178:181], v[58:61]
	v_mfma_f32_16x16x32_bf16 v[46:49], v[142:145], v[186:189], v[46:49]
	v_mfma_f32_16x16x32_bf16 v[42:45], v[150:153], v[186:189], v[42:45]
	v_mfma_f32_16x16x32_bf16 v[30:33], v[142:145], v[194:197], v[30:33]
	v_mfma_f32_16x16x32_bf16 v[26:29], v[150:153], v[194:197], v[26:29]
	v_mfma_f32_16x16x32_bf16 v[14:17], v[142:145], v[202:205], v[14:17]
	v_mfma_f32_16x16x32_bf16 v[10:13], v[150:153], v[202:205], v[10:13]
	v_mfma_f32_16x16x32_bf16 v[62:65], v[146:149], v[182:185], v[62:65]
	v_mfma_f32_16x16x32_bf16 v[58:61], v[154:157], v[182:185], v[58:61]
	v_mfma_f32_16x16x32_bf16 v[46:49], v[146:149], v[190:193], v[46:49]
	v_mfma_f32_16x16x32_bf16 v[42:45], v[154:157], v[190:193], v[42:45]
	v_mfma_f32_16x16x32_bf16 v[30:33], v[146:149], v[198:201], v[30:33]
	v_mfma_f32_16x16x32_bf16 v[26:29], v[154:157], v[198:201], v[26:29]
	v_mfma_f32_16x16x32_bf16 v[14:17], v[146:149], v[206:209], v[14:17]
	v_mfma_f32_16x16x32_bf16 v[10:13], v[154:157], v[206:209], v[10:13]
	v_mfma_f32_16x16x32_bf16 v[54:57], v[158:161], v[178:181], v[54:57]
	v_mfma_f32_16x16x32_bf16 v[50:53], v[166:169], v[178:181], v[50:53]
	v_mfma_f32_16x16x32_bf16 v[38:41], v[158:161], v[186:189], v[38:41]
	v_mfma_f32_16x16x32_bf16 v[34:37], v[166:169], v[186:189], v[34:37]
	v_mfma_f32_16x16x32_bf16 v[22:25], v[158:161], v[194:197], v[22:25]
	v_mfma_f32_16x16x32_bf16 v[18:21], v[166:169], v[194:197], v[18:21]
	v_mfma_f32_16x16x32_bf16 v[6:9], v[158:161], v[202:205], v[6:9]
	v_mfma_f32_16x16x32_bf16 v[2:5], v[166:169], v[202:205], v[2:5]
	v_mfma_f32_16x16x32_bf16 v[54:57], v[162:165], v[182:185], v[54:57]
	v_mfma_f32_16x16x32_bf16 v[50:53], v[174:177], v[182:185], v[50:53]
	v_mfma_f32_16x16x32_bf16 v[38:41], v[162:165], v[190:193], v[38:41]
	v_mfma_f32_16x16x32_bf16 v[34:37], v[174:177], v[190:193], v[34:37]
	v_mfma_f32_16x16x32_bf16 v[22:25], v[162:165], v[198:201], v[22:25]
	v_mfma_f32_16x16x32_bf16 v[18:21], v[174:177], v[198:201], v[18:21]
	v_mfma_f32_16x16x32_bf16 v[6:9], v[162:165], v[206:209], v[6:9]
	v_mfma_f32_16x16x32_bf16 v[2:5], v[174:177], v[206:209], v[2:5]
	s_barrier
.Lmid170:
	ds_read_b128 v[142:145], v139
	ds_read_b128 v[146:149], v139 offset:1024
	ds_read_b128 v[150:153], v139 offset:2048
	ds_read_b128 v[154:157], v139 offset:3072
	ds_read_b128 v[158:161], v140
	ds_read_b128 v[162:165], v140 offset:1024
	ds_read_b128 v[166:169], v140 offset:2048
	ds_read_b128 v[174:177], v140 offset:3072
	ds_read_b128 v[178:181], v138 offset:32768
	ds_read_b128 v[182:185], v138 offset:33792
	ds_read_b128 v[186:189], v138 offset:34816
	ds_read_b128 v[190:193], v138 offset:35840
	ds_read_b128 v[194:197], v138 offset:36864
	ds_read_b128 v[198:201], v138 offset:37888
	ds_read_b128 v[202:205], v138 offset:38912
	ds_read_b128 v[206:209], v138 offset:39936
	s_add_u32 s12, s20, 0x40000
	s_addc_u32 s13, s21, 0
	s_mov_b32 s20, m0
	s_mov_b32 m0, s31
	s_nop 2
	global_load_lds_dwordx4 v132, s[12:13]
	s_mov_b32 m0, s20
	s_nop 0
	s_mov_b32 s20, m0
	s_mov_b32 m0, s33
	s_nop 2
	global_load_lds_dwordx4 v134, s[12:13]
	s_mov_b32 m0, s20
	s_waitcnt vmcnt(8)
	s_waitcnt lgkmcnt(0)
	s_barrier
	v_mfma_f32_16x16x32_bf16 v[126:129], v[142:145], v[178:181], v[126:129]
	v_mfma_f32_16x16x32_bf16 v[122:125], v[150:153], v[178:181], v[122:125]
	v_mfma_f32_16x16x32_bf16 v[110:113], v[142:145], v[186:189], v[110:113]
	v_mfma_f32_16x16x32_bf16 v[106:109], v[150:153], v[186:189], v[106:109]
	v_mfma_f32_16x16x32_bf16 v[94:97], v[142:145], v[194:197], v[94:97]
	v_mfma_f32_16x16x32_bf16 v[90:93], v[150:153], v[194:197], v[90:93]
	v_mfma_f32_16x16x32_bf16 v[78:81], v[142:145], v[202:205], v[78:81]
	v_mfma_f32_16x16x32_bf16 v[74:77], v[150:153], v[202:205], v[74:77]
	v_mfma_f32_16x16x32_bf16 v[126:129], v[146:149], v[182:185], v[126:129]
	v_mfma_f32_16x16x32_bf16 v[122:125], v[154:157], v[182:185], v[122:125]
	v_mfma_f32_16x16x32_bf16 v[110:113], v[146:149], v[190:193], v[110:113]
	v_mfma_f32_16x16x32_bf16 v[106:109], v[154:157], v[190:193], v[106:109]
	v_mfma_f32_16x16x32_bf16 v[94:97], v[146:149], v[198:201], v[94:97]
	v_mfma_f32_16x16x32_bf16 v[90:93], v[154:157], v[198:201], v[90:93]
	v_mfma_f32_16x16x32_bf16 v[78:81], v[146:149], v[206:209], v[78:81]
	v_mfma_f32_16x16x32_bf16 v[74:77], v[154:157], v[206:209], v[74:77]
	v_mfma_f32_16x16x32_bf16 v[118:121], v[158:161], v[178:181], v[118:121]
	v_mfma_f32_16x16x32_bf16 v[114:117], v[166:169], v[178:181], v[114:117]
	v_mfma_f32_16x16x32_bf16 v[102:105], v[158:161], v[186:189], v[102:105]
	v_mfma_f32_16x16x32_bf16 v[98:101], v[166:169], v[186:189], v[98:101]
	v_mfma_f32_16x16x32_bf16 v[86:89], v[158:161], v[194:197], v[86:89]
	v_mfma_f32_16x16x32_bf16 v[82:85], v[166:169], v[194:197], v[82:85]
	v_mfma_f32_16x16x32_bf16 v[70:73], v[158:161], v[202:205], v[70:73]
	v_mfma_f32_16x16x32_bf16 v[66:69], v[166:169], v[202:205], v[66:69]
	v_mfma_f32_16x16x32_bf16 v[118:121], v[162:165], v[182:185], v[118:121]
	v_mfma_f32_16x16x32_bf16 v[114:117], v[174:177], v[182:185], v[114:117]
	v_mfma_f32_16x16x32_bf16 v[102:105], v[162:165], v[190:193], v[102:105]
	v_mfma_f32_16x16x32_bf16 v[98:101], v[174:177], v[190:193], v[98:101]
	v_mfma_f32_16x16x32_bf16 v[86:89], v[162:165], v[198:201], v[86:89]
	v_mfma_f32_16x16x32_bf16 v[82:85], v[174:177], v[198:201], v[82:85]
	v_mfma_f32_16x16x32_bf16 v[70:73], v[162:165], v[206:209], v[70:73]
	v_mfma_f32_16x16x32_bf16 v[66:69], v[174:177], v[206:209], v[66:69]
	s_barrier
	ds_read_b128 v[178:181], v138 offset:49152
	ds_read_b128 v[182:185], v138 offset:50176
	ds_read_b128 v[186:189], v138 offset:51200
	ds_read_b128 v[190:193], v138 offset:52224
	ds_read_b128 v[194:197], v138 offset:53248
	ds_read_b128 v[198:201], v138 offset:54272
	ds_read_b128 v[202:205], v138 offset:55296
	ds_read_b128 v[206:209], v138 offset:56320
	s_add_u32 s12, s18, 0x80
	s_addc_u32 s13, s19, 0
	s_mov_b32 s20, m0
	s_mov_b32 m0, s34
	s_nop 2
	global_load_lds_dwordx4 v133, s[12:13]
	s_mov_b32 m0, s20
	s_nop 0
	s_mov_b32 s20, m0
	s_mov_b32 m0, s35
	s_nop 2
	global_load_lds_dwordx4 v135, s[12:13]
	s_mov_b32 m0, s20
	s_add_u32 s12, s18, 0x40080
	s_addc_u32 s13, s19, 0
	s_mov_b32 s18, m0
	s_mov_b32 m0, s40
	s_nop 2
	global_load_lds_dwordx4 v133, s[12:13]
	s_mov_b32 m0, s18
	s_nop 0
	s_mov_b32 s18, m0
	s_mov_b32 m0, s41
	s_nop 2
	global_load_lds_dwordx4 v135, s[12:13]
	s_mov_b32 m0, s18
	s_mov_b32 s12, m0
	s_mov_b32 m0, s36
	s_nop 2
	global_load_lds_dwordx4 v132, s[16:17]
	s_mov_b32 m0, s12
	s_nop 0
	s_mov_b32 s12, m0
	s_mov_b32 m0, s37
	s_nop 2
	global_load_lds_dwordx4 v134, s[16:17]
	s_mov_b32 m0, s12
	s_waitcnt vmcnt(8)
	s_waitcnt lgkmcnt(0)
	s_barrier
	v_mfma_f32_16x16x32_bf16 v[62:65], v[142:145], v[178:181], v[62:65]
	v_mfma_f32_16x16x32_bf16 v[58:61], v[150:153], v[178:181], v[58:61]
	v_mfma_f32_16x16x32_bf16 v[46:49], v[142:145], v[186:189], v[46:49]
	v_mfma_f32_16x16x32_bf16 v[42:45], v[150:153], v[186:189], v[42:45]
	v_mfma_f32_16x16x32_bf16 v[30:33], v[142:145], v[194:197], v[30:33]
	v_mfma_f32_16x16x32_bf16 v[26:29], v[150:153], v[194:197], v[26:29]
	v_mfma_f32_16x16x32_bf16 v[14:17], v[142:145], v[202:205], v[14:17]
	v_mfma_f32_16x16x32_bf16 v[10:13], v[150:153], v[202:205], v[10:13]
	v_mfma_f32_16x16x32_bf16 v[62:65], v[146:149], v[182:185], v[62:65]
	v_mfma_f32_16x16x32_bf16 v[58:61], v[154:157], v[182:185], v[58:61]
	v_mfma_f32_16x16x32_bf16 v[46:49], v[146:149], v[190:193], v[46:49]
	v_mfma_f32_16x16x32_bf16 v[42:45], v[154:157], v[190:193], v[42:45]
	v_mfma_f32_16x16x32_bf16 v[30:33], v[146:149], v[198:201], v[30:33]
	v_mfma_f32_16x16x32_bf16 v[26:29], v[154:157], v[198:201], v[26:29]
	v_mfma_f32_16x16x32_bf16 v[14:17], v[146:149], v[206:209], v[14:17]
	v_mfma_f32_16x16x32_bf16 v[10:13], v[154:157], v[206:209], v[10:13]
	v_mfma_f32_16x16x32_bf16 v[54:57], v[158:161], v[178:181], v[54:57]
	v_mfma_f32_16x16x32_bf16 v[50:53], v[166:169], v[178:181], v[50:53]
	v_mfma_f32_16x16x32_bf16 v[38:41], v[158:161], v[186:189], v[38:41]
	v_mfma_f32_16x16x32_bf16 v[34:37], v[166:169], v[186:189], v[34:37]
	v_mfma_f32_16x16x32_bf16 v[22:25], v[158:161], v[194:197], v[22:25]
	v_mfma_f32_16x16x32_bf16 v[18:21], v[166:169], v[194:197], v[18:21]
	v_mfma_f32_16x16x32_bf16 v[6:9], v[158:161], v[202:205], v[6:9]
	v_mfma_f32_16x16x32_bf16 v[2:5], v[166:169], v[202:205], v[2:5]
	v_mfma_f32_16x16x32_bf16 v[54:57], v[162:165], v[182:185], v[54:57]
	v_mfma_f32_16x16x32_bf16 v[50:53], v[174:177], v[182:185], v[50:53]
	v_mfma_f32_16x16x32_bf16 v[38:41], v[162:165], v[190:193], v[38:41]
	v_mfma_f32_16x16x32_bf16 v[34:37], v[174:177], v[190:193], v[34:37]
	v_mfma_f32_16x16x32_bf16 v[22:25], v[162:165], v[198:201], v[22:25]
	v_mfma_f32_16x16x32_bf16 v[18:21], v[174:177], v[198:201], v[18:21]
	v_mfma_f32_16x16x32_bf16 v[6:9], v[162:165], v[206:209], v[6:9]
	v_mfma_f32_16x16x32_bf16 v[2:5], v[174:177], v[206:209], v[2:5]
	s_barrier
	s_add_i32 s56, s56, 2
	s_add_u32 s54, s54, 0x100
	s_addc_u32 s55, s55, 0
	s_cmp_gt_u32 s56, 13
	s_mov_b64 s[12:13], s[14:15]
	s_cbranch_scc0 .LBB0_170
	s_cmpk_lt_u32 s23, 0x100
	s_cbranch_scc0 .LBB0_173
	s_barrier

.Lpeel1046:
	ds_read_b128 v[136:139], v172
	ds_read_b128 v[140:143], v172 offset:1024
	ds_read_b128 v[144:147], v172 offset:2048
	ds_read_b128 v[148:151], v172 offset:3072
	ds_read_b128 v[152:155], v173
	ds_read_b128 v[156:159], v173 offset:1024
	ds_read_b128 v[160:163], v173 offset:2048
	ds_read_b128 v[178:181], v173 offset:3072
	s_add_u32 s25, s64, s56
	s_addc_u32 s33, s65, s57
	s_add_u32 s66, s25, 0x100
	s_addc_u32 s67, s33, 0
	s_add_u32 s23, s62, s56
	s_addc_u32 s24, s63, s57
	s_add_u32 s28, s23, 0x100
	s_addc_u32 s29, s24, 0
	s_add_u32 s58, s25, 0x180
	s_addc_u32 s59, s33, 0
	ds_read_b128 v[182:185], v174
	ds_read_b128 v[186:189], v174 offset:1024
	ds_read_b128 v[190:193], v174 offset:2048
	ds_read_b128 v[194:197], v174 offset:3072
	ds_read_b128 v[198:201], v174 offset:4096
	ds_read_b128 v[202:205], v174 offset:5120
	ds_read_b128 v[206:209], v174 offset:6144
	ds_read_b128 v[210:213], v174 offset:7168
	s_add_u32 s30, s25, 0x40080
	s_addc_u32 s31, s33, 0
	s_mov_b32 s36, m0
	s_mov_b32 m0, s26
	s_nop 2
	global_load_lds_dwordx4 v165, s[30:31]
	s_mov_b32 m0, s36
	s_nop 0
	s_mov_b32 s36, m0
	s_mov_b32 m0, s27
	s_nop 2
	global_load_lds_dwordx4 v167, s[30:31]
	s_mov_b32 m0, s36
	s_waitcnt vmcnt(8)
	s_waitcnt lgkmcnt(0)
	s_barrier
	v_mfma_f32_16x16x32_bf16 v[26:29], v[136:139], v[182:185], 0
	v_mfma_f32_16x16x32_bf16 v[30:33], v[144:147], v[182:185], 0
	v_mfma_f32_16x16x32_bf16 v[50:53], v[136:139], v[190:193], 0
	v_mfma_f32_16x16x32_bf16 v[54:57], v[144:147], v[190:193], 0
	v_mfma_f32_16x16x32_bf16 v[74:77], v[136:139], v[198:201], 0
	v_mfma_f32_16x16x32_bf16 v[78:81], v[144:147], v[198:201], 0
	v_mfma_f32_16x16x32_bf16 v[94:97], v[136:139], v[206:209], 0
	v_mfma_f32_16x16x32_bf16 v[102:105], v[144:147], v[206:209], 0
	v_mfma_f32_16x16x32_bf16 v[26:29], v[140:143], v[186:189], v[26:29]
	v_mfma_f32_16x16x32_bf16 v[30:33], v[148:151], v[186:189], v[30:33]
	v_mfma_f32_16x16x32_bf16 v[50:53], v[140:143], v[194:197], v[50:53]
	v_mfma_f32_16x16x32_bf16 v[54:57], v[148:151], v[194:197], v[54:57]
	v_mfma_f32_16x16x32_bf16 v[74:77], v[140:143], v[202:205], v[74:77]
	v_mfma_f32_16x16x32_bf16 v[78:81], v[148:151], v[202:205], v[78:81]
	v_mfma_f32_16x16x32_bf16 v[94:97], v[140:143], v[210:213], v[94:97]
	v_mfma_f32_16x16x32_bf16 v[102:105], v[148:151], v[210:213], v[102:105]
	v_mfma_f32_16x16x32_bf16 v[38:41], v[152:155], v[182:185], 0
	v_mfma_f32_16x16x32_bf16 v[42:45], v[160:163], v[182:185], 0
	v_mfma_f32_16x16x32_bf16 v[62:65], v[152:155], v[190:193], 0
	v_mfma_f32_16x16x32_bf16 v[66:69], v[160:163], v[190:193], 0
	v_mfma_f32_16x16x32_bf16 v[82:85], v[152:155], v[198:201], 0
	v_mfma_f32_16x16x32_bf16 v[90:93], v[160:163], v[198:201], 0
	v_mfma_f32_16x16x32_bf16 v[106:109], v[152:155], v[206:209], 0
	v_mfma_f32_16x16x32_bf16 v[114:117], v[160:163], v[206:209], 0
	v_mfma_f32_16x16x32_bf16 v[38:41], v[156:159], v[186:189], v[38:41]
	v_mfma_f32_16x16x32_bf16 v[42:45], v[178:181], v[186:189], v[42:45]
	v_mfma_f32_16x16x32_bf16 v[62:65], v[156:159], v[194:197], v[62:65]
	v_mfma_f32_16x16x32_bf16 v[66:69], v[178:181], v[194:197], v[66:69]
	v_mfma_f32_16x16x32_bf16 v[82:85], v[156:159], v[202:205], v[82:85]
	v_mfma_f32_16x16x32_bf16 v[90:93], v[178:181], v[202:205], v[90:93]
	v_mfma_f32_16x16x32_bf16 v[106:109], v[156:159], v[210:213], v[106:109]
	v_mfma_f32_16x16x32_bf16 v[114:117], v[178:181], v[210:213], v[114:117]
	s_barrier
	ds_read_b128 v[182:185], v174 offset:16384
	ds_read_b128 v[186:189], v174 offset:17408
	ds_read_b128 v[190:193], v174 offset:18432
	ds_read_b128 v[194:197], v174 offset:19456
	ds_read_b128 v[198:201], v174 offset:20480
	ds_read_b128 v[202:205], v174 offset:21504
	ds_read_b128 v[206:209], v174 offset:22528
	ds_read_b128 v[210:213], v174 offset:23552
	s_mov_b32 s30, m0
	s_mov_b32 m0, s80
	s_nop 2
	global_load_lds_dwordx4 v166, s[28:29]
	s_mov_b32 m0, s30
	s_nop 0
	s_mov_b32 s30, m0
	s_mov_b32 m0, s81
	s_nop 2
	global_load_lds_dwordx4 v168, s[28:29]
	s_mov_b32 m0, s30
	s_add_u32 s28, s23, 0x40100
	s_addc_u32 s29, s24, 0
	s_mov_b32 s30, m0
	s_mov_b32 m0, s82
	s_nop 2
	global_load_lds_dwordx4 v166, s[28:29]
	s_mov_b32 m0, s30
	s_nop 0
	s_mov_b32 s30, m0
	s_mov_b32 m0, s83
	s_nop 2
	global_load_lds_dwordx4 v168, s[28:29]
	s_mov_b32 m0, s30
	s_mov_b32 s28, m0
	s_mov_b32 m0, s79
	s_nop 2
	global_load_lds_dwordx4 v165, s[66:67]
	s_mov_b32 m0, s28
	s_nop 0
	s_mov_b32 s28, m0
	s_mov_b32 m0, s84
	s_nop 2
	global_load_lds_dwordx4 v167, s[66:67]
	s_mov_b32 m0, s28
	s_waitcnt vmcnt(8)
	s_waitcnt lgkmcnt(0)
	s_barrier
	v_mfma_f32_16x16x32_bf16 v[118:121], v[136:139], v[182:185], 0
	v_mfma_f32_16x16x32_bf16 v[126:129], v[144:147], v[182:185], 0
	v_mfma_f32_16x16x32_bf16 v[98:101], v[136:139], v[190:193], 0
	v_mfma_f32_16x16x32_bf16 v[86:89], v[144:147], v[190:193], 0
	v_mfma_f32_16x16x32_bf16 v[46:49], v[136:139], v[198:201], 0
	v_mfma_f32_16x16x32_bf16 v[34:37], v[144:147], v[198:201], 0
	v_mfma_f32_16x16x32_bf16 v[14:17], v[136:139], v[206:209], 0
	v_mfma_f32_16x16x32_bf16 v[10:13], v[144:147], v[206:209], 0
	v_mfma_f32_16x16x32_bf16 v[118:121], v[140:143], v[186:189], v[118:121]
	v_mfma_f32_16x16x32_bf16 v[126:129], v[148:151], v[186:189], v[126:129]
	v_mfma_f32_16x16x32_bf16 v[98:101], v[140:143], v[194:197], v[98:101]
	v_mfma_f32_16x16x32_bf16 v[86:89], v[148:151], v[194:197], v[86:89]
	v_mfma_f32_16x16x32_bf16 v[46:49], v[140:143], v[202:205], v[46:49]
	v_mfma_f32_16x16x32_bf16 v[34:37], v[148:151], v[202:205], v[34:37]
	v_mfma_f32_16x16x32_bf16 v[14:17], v[140:143], v[210:213], v[14:17]
	v_mfma_f32_16x16x32_bf16 v[10:13], v[148:151], v[210:213], v[10:13]
	v_mfma_f32_16x16x32_bf16 v[122:125], v[152:155], v[182:185], 0
	v_mfma_f32_16x16x32_bf16 v[110:113], v[160:163], v[182:185], 0
	v_mfma_f32_16x16x32_bf16 v[70:73], v[152:155], v[190:193], 0
	v_mfma_f32_16x16x32_bf16 v[58:61], v[160:163], v[190:193], 0
	v_mfma_f32_16x16x32_bf16 v[22:25], v[152:155], v[198:201], 0
	v_mfma_f32_16x16x32_bf16 v[18:21], v[160:163], v[198:201], 0
	v_mfma_f32_16x16x32_bf16 v[6:9], v[152:155], v[206:209], 0
	v_mfma_f32_16x16x32_bf16 v[2:5], v[160:163], v[206:209], 0
	v_mfma_f32_16x16x32_bf16 v[122:125], v[156:159], v[186:189], v[122:125]
	v_mfma_f32_16x16x32_bf16 v[110:113], v[178:181], v[186:189], v[110:113]
	v_mfma_f32_16x16x32_bf16 v[70:73], v[156:159], v[194:197], v[70:73]
	v_mfma_f32_16x16x32_bf16 v[58:61], v[178:181], v[194:197], v[58:61]
	v_mfma_f32_16x16x32_bf16 v[22:25], v[156:159], v[202:205], v[22:25]
	v_mfma_f32_16x16x32_bf16 v[18:21], v[178:181], v[202:205], v[18:21]
	v_mfma_f32_16x16x32_bf16 v[6:9], v[156:159], v[210:213], v[6:9]
	v_mfma_f32_16x16x32_bf16 v[2:5], v[178:181], v[210:213], v[2:5]
	s_barrier
	s_branch .Lmid1046
.LBB0_1046:
	ds_read_b128 v[136:139], v172
	ds_read_b128 v[140:143], v172 offset:1024
	ds_read_b128 v[144:147], v172 offset:2048
	ds_read_b128 v[148:151], v172 offset:3072
	ds_read_b128 v[152:155], v173
	ds_read_b128 v[156:159], v173 offset:1024
	ds_read_b128 v[160:163], v173 offset:2048
	ds_read_b128 v[178:181], v173 offset:3072
	s_add_u32 s25, s64, s56
	s_addc_u32 s33, s65, s57
	s_add_u32 s66, s25, 0x100
	s_addc_u32 s67, s33, 0
	s_add_u32 s23, s62, s56
	s_addc_u32 s24, s63, s57
	s_add_u32 s28, s23, 0x100
	s_addc_u32 s29, s24, 0
	s_add_u32 s58, s25, 0x180
	s_addc_u32 s59, s33, 0
	ds_read_b128 v[182:185], v174
	ds_read_b128 v[186:189], v174 offset:1024
	ds_read_b128 v[190:193], v174 offset:2048
	ds_read_b128 v[194:197], v174 offset:3072
	ds_read_b128 v[198:201], v174 offset:4096
	ds_read_b128 v[202:205], v174 offset:5120
	ds_read_b128 v[206:209], v174 offset:6144
	ds_read_b128 v[210:213], v174 offset:7168
	s_add_u32 s30, s25, 0x40080
	s_addc_u32 s31, s33, 0
	s_mov_b32 s36, m0
	s_mov_b32 m0, s26
	s_nop 2
	global_load_lds_dwordx4 v165, s[30:31]
	s_mov_b32 m0, s36
	s_nop 0
	s_mov_b32 s36, m0
	s_mov_b32 m0, s27
	s_nop 2
	global_load_lds_dwordx4 v167, s[30:31]
	s_mov_b32 m0, s36
	s_waitcnt vmcnt(8)
	s_waitcnt lgkmcnt(0)
	s_barrier
	v_mfma_f32_16x16x32_bf16 v[26:29], v[136:139], v[182:185], v[26:29]
	v_mfma_f32_16x16x32_bf16 v[30:33], v[144:147], v[182:185], v[30:33]
	v_mfma_f32_16x16x32_bf16 v[50:53], v[136:139], v[190:193], v[50:53]
	v_mfma_f32_16x16x32_bf16 v[54:57], v[144:147], v[190:193], v[54:57]
	v_mfma_f32_16x16x32_bf16 v[74:77], v[136:139], v[198:201], v[74:77]
	v_mfma_f32_16x16x32_bf16 v[78:81], v[144:147], v[198:201], v[78:81]
	v_mfma_f32_16x16x32_bf16 v[94:97], v[136:139], v[206:209], v[94:97]
	v_mfma_f32_16x16x32_bf16 v[102:105], v[144:147], v[206:209], v[102:105]
	v_mfma_f32_16x16x32_bf16 v[26:29], v[140:143], v[186:189], v[26:29]
	v_mfma_f32_16x16x32_bf16 v[30:33], v[148:151], v[186:189], v[30:33]
	v_mfma_f32_16x16x32_bf16 v[50:53], v[140:143], v[194:197], v[50:53]
	v_mfma_f32_16x16x32_bf16 v[54:57], v[148:151], v[194:197], v[54:57]
	v_mfma_f32_16x16x32_bf16 v[74:77], v[140:143], v[202:205], v[74:77]
	v_mfma_f32_16x16x32_bf16 v[78:81], v[148:151], v[202:205], v[78:81]
	v_mfma_f32_16x16x32_bf16 v[94:97], v[140:143], v[210:213], v[94:97]
	v_mfma_f32_16x16x32_bf16 v[102:105], v[148:151], v[210:213], v[102:105]
	v_mfma_f32_16x16x32_bf16 v[38:41], v[152:155], v[182:185], v[38:41]
	v_mfma_f32_16x16x32_bf16 v[42:45], v[160:163], v[182:185], v[42:45]
	v_mfma_f32_16x16x32_bf16 v[62:65], v[152:155], v[190:193], v[62:65]
	v_mfma_f32_16x16x32_bf16 v[66:69], v[160:163], v[190:193], v[66:69]
	v_mfma_f32_16x16x32_bf16 v[82:85], v[152:155], v[198:201], v[82:85]
	v_mfma_f32_16x16x32_bf16 v[90:93], v[160:163], v[198:201], v[90:93]
	v_mfma_f32_16x16x32_bf16 v[106:109], v[152:155], v[206:209], v[106:109]
	v_mfma_f32_16x16x32_bf16 v[114:117], v[160:163], v[206:209], v[114:117]
	v_mfma_f32_16x16x32_bf16 v[38:41], v[156:159], v[186:189], v[38:41]
	v_mfma_f32_16x16x32_bf16 v[42:45], v[178:181], v[186:189], v[42:45]
	v_mfma_f32_16x16x32_bf16 v[62:65], v[156:159], v[194:197], v[62:65]
	v_mfma_f32_16x16x32_bf16 v[66:69], v[178:181], v[194:197], v[66:69]
	v_mfma_f32_16x16x32_bf16 v[82:85], v[156:159], v[202:205], v[82:85]
	v_mfma_f32_16x16x32_bf16 v[90:93], v[178:181], v[202:205], v[90:93]
	v_mfma_f32_16x16x32_bf16 v[106:109], v[156:159], v[210:213], v[106:109]
	v_mfma_f32_16x16x32_bf16 v[114:117], v[178:181], v[210:213], v[114:117]
	s_barrier
	ds_read_b128 v[182:185], v174 offset:16384
	ds_read_b128 v[186:189], v174 offset:17408
	ds_read_b128 v[190:193], v174 offset:18432
	ds_read_b128 v[194:197], v174 offset:19456
	ds_read_b128 v[198:201], v174 offset:20480
	ds_read_b128 v[202:205], v174 offset:21504
	ds_read_b128 v[206:209], v174 offset:22528
	ds_read_b128 v[210:213], v174 offset:23552
	s_mov_b32 s30, m0
	s_mov_b32 m0, s80
	s_nop 2
	global_load_lds_dwordx4 v166, s[28:29]
	s_mov_b32 m0, s30
	s_nop 0
	s_mov_b32 s30, m0
	s_mov_b32 m0, s81
	s_nop 2
	global_load_lds_dwordx4 v168, s[28:29]
	s_mov_b32 m0, s30
	s_add_u32 s28, s23, 0x40100
	s_addc_u32 s29, s24, 0
	s_mov_b32 s30, m0
	s_mov_b32 m0, s82
	s_nop 2
	global_load_lds_dwordx4 v166, s[28:29]
	s_mov_b32 m0, s30
	s_nop 0
	s_mov_b32 s30, m0
	s_mov_b32 m0, s83
	s_nop 2
	global_load_lds_dwordx4 v168, s[28:29]
	s_mov_b32 m0, s30
	s_mov_b32 s28, m0
	s_mov_b32 m0, s79
	s_nop 2
	global_load_lds_dwordx4 v165, s[66:67]
	s_mov_b32 m0, s28
	s_nop 0
	s_mov_b32 s28, m0
	s_mov_b32 m0, s84
	s_nop 2
	global_load_lds_dwordx4 v167, s[66:67]
	s_mov_b32 m0, s28
	s_waitcnt vmcnt(8)
	s_waitcnt lgkmcnt(0)
	s_barrier
	v_mfma_f32_16x16x32_bf16 v[118:121], v[136:139], v[182:185], v[118:121]
	v_mfma_f32_16x16x32_bf16 v[126:129], v[144:147], v[182:185], v[126:129]
	v_mfma_f32_16x16x32_bf16 v[98:101], v[136:139], v[190:193], v[98:101]
	v_mfma_f32_16x16x32_bf16 v[86:89], v[144:147], v[190:193], v[86:89]
	v_mfma_f32_16x16x32_bf16 v[46:49], v[136:139], v[198:201], v[46:49]
	v_mfma_f32_16x16x32_bf16 v[34:37], v[144:147], v[198:201], v[34:37]
	v_mfma_f32_16x16x32_bf16 v[14:17], v[136:139], v[206:209], v[14:17]
	v_mfma_f32_16x16x32_bf16 v[10:13], v[144:147], v[206:209], v[10:13]
	v_mfma_f32_16x16x32_bf16 v[118:121], v[140:143], v[186:189], v[118:121]
	v_mfma_f32_16x16x32_bf16 v[126:129], v[148:151], v[186:189], v[126:129]
	v_mfma_f32_16x16x32_bf16 v[98:101], v[140:143], v[194:197], v[98:101]
	v_mfma_f32_16x16x32_bf16 v[86:89], v[148:151], v[194:197], v[86:89]
	v_mfma_f32_16x16x32_bf16 v[46:49], v[140:143], v[202:205], v[46:49]
	v_mfma_f32_16x16x32_bf16 v[34:37], v[148:151], v[202:205], v[34:37]
	v_mfma_f32_16x16x32_bf16 v[14:17], v[140:143], v[210:213], v[14:17]
	v_mfma_f32_16x16x32_bf16 v[10:13], v[148:151], v[210:213], v[10:13]
	v_mfma_f32_16x16x32_bf16 v[122:125], v[152:155], v[182:185], v[122:125]
	v_mfma_f32_16x16x32_bf16 v[110:113], v[160:163], v[182:185], v[110:113]
	v_mfma_f32_16x16x32_bf16 v[70:73], v[152:155], v[190:193], v[70:73]
	v_mfma_f32_16x16x32_bf16 v[58:61], v[160:163], v[190:193], v[58:61]
	v_mfma_f32_16x16x32_bf16 v[22:25], v[152:155], v[198:201], v[22:25]
	v_mfma_f32_16x16x32_bf16 v[18:21], v[160:163], v[198:201], v[18:21]
	v_mfma_f32_16x16x32_bf16 v[6:9], v[152:155], v[206:209], v[6:9]
	v_mfma_f32_16x16x32_bf16 v[2:5], v[160:163], v[206:209], v[2:5]
	v_mfma_f32_16x16x32_bf16 v[122:125], v[156:159], v[186:189], v[122:125]
	v_mfma_f32_16x16x32_bf16 v[110:113], v[178:181], v[186:189], v[110:113]
	v_mfma_f32_16x16x32_bf16 v[70:73], v[156:159], v[194:197], v[70:73]
	v_mfma_f32_16x16x32_bf16 v[58:61], v[178:181], v[194:197], v[58:61]
	v_mfma_f32_16x16x32_bf16 v[22:25], v[156:159], v[202:205], v[22:25]
	v_mfma_f32_16x16x32_bf16 v[18:21], v[178:181], v[202:205], v[18:21]
	v_mfma_f32_16x16x32_bf16 v[6:9], v[156:159], v[210:213], v[6:9]
	v_mfma_f32_16x16x32_bf16 v[2:5], v[178:181], v[210:213], v[2:5]
	s_barrier
.Lmid1046:
	ds_read_b128 v[136:139], v175
	ds_read_b128 v[140:143], v175 offset:1024
	ds_read_b128 v[144:147], v175 offset:2048
	ds_read_b128 v[148:151], v175 offset:3072
	ds_read_b128 v[152:155], v176
	ds_read_b128 v[156:159], v176 offset:1024
	ds_read_b128 v[160:163], v176 offset:2048
	ds_read_b128 v[178:181], v176 offset:3072
	ds_read_b128 v[182:185], v174 offset:32768
	ds_read_b128 v[186:189], v174 offset:33792
	ds_read_b128 v[190:193], v174 offset:34816
	ds_read_b128 v[194:197], v174 offset:35840
	ds_read_b128 v[198:201], v174 offset:36864
	ds_read_b128 v[202:205], v174 offset:37888
	ds_read_b128 v[206:209], v174 offset:38912
	ds_read_b128 v[210:213], v174 offset:39936
	s_add_u32 s28, s25, 0x40100
	s_addc_u32 s29, s33, 0
	s_mov_b32 s25, m0
	s_mov_b32 m0, s85
	s_nop 2
	global_load_lds_dwordx4 v165, s[28:29]
	s_mov_b32 m0, s25
	s_nop 0
	s_mov_b32 s25, m0
	s_mov_b32 m0, s86
	s_nop 2
	global_load_lds_dwordx4 v167, s[28:29]
	s_mov_b32 m0, s25
	s_waitcnt vmcnt(8)
	s_waitcnt lgkmcnt(0)
	s_barrier
	v_mfma_f32_16x16x32_bf16 v[26:29], v[136:139], v[182:185], v[26:29]
	v_mfma_f32_16x16x32_bf16 v[30:33], v[144:147], v[182:185], v[30:33]
	v_mfma_f32_16x16x32_bf16 v[50:53], v[136:139], v[190:193], v[50:53]
	v_mfma_f32_16x16x32_bf16 v[54:57], v[144:147], v[190:193], v[54:57]
	v_mfma_f32_16x16x32_bf16 v[74:77], v[136:139], v[198:201], v[74:77]
	v_mfma_f32_16x16x32_bf16 v[78:81], v[144:147], v[198:201], v[78:81]
	v_mfma_f32_16x16x32_bf16 v[94:97], v[136:139], v[206:209], v[94:97]
	v_mfma_f32_16x16x32_bf16 v[102:105], v[144:147], v[206:209], v[102:105]
	v_mfma_f32_16x16x32_bf16 v[26:29], v[140:143], v[186:189], v[26:29]
	v_mfma_f32_16x16x32_bf16 v[30:33], v[148:151], v[186:189], v[30:33]
	v_mfma_f32_16x16x32_bf16 v[50:53], v[140:143], v[194:197], v[50:53]
	v_mfma_f32_16x16x32_bf16 v[54:57], v[148:151], v[194:197], v[54:57]
	v_mfma_f32_16x16x32_bf16 v[74:77], v[140:143], v[202:205], v[74:77]
	v_mfma_f32_16x16x32_bf16 v[78:81], v[148:151], v[202:205], v[78:81]
	v_mfma_f32_16x16x32_bf16 v[94:97], v[140:143], v[210:213], v[94:97]
	v_mfma_f32_16x16x32_bf16 v[102:105], v[148:151], v[210:213], v[102:105]
	v_mfma_f32_16x16x32_bf16 v[38:41], v[152:155], v[182:185], v[38:41]
	v_mfma_f32_16x16x32_bf16 v[42:45], v[160:163], v[182:185], v[42:45]
	v_mfma_f32_16x16x32_bf16 v[62:65], v[152:155], v[190:193], v[62:65]
	v_mfma_f32_16x16x32_bf16 v[66:69], v[160:163], v[190:193], v[66:69]
	v_mfma_f32_16x16x32_bf16 v[82:85], v[152:155], v[198:201], v[82:85]
	v_mfma_f32_16x16x32_bf16 v[90:93], v[160:163], v[198:201], v[90:93]
	v_mfma_f32_16x16x32_bf16 v[106:109], v[152:155], v[206:209], v[106:109]
	v_mfma_f32_16x16x32_bf16 v[114:117], v[160:163], v[206:209], v[114:117]
	v_mfma_f32_16x16x32_bf16 v[38:41], v[156:159], v[186:189], v[38:41]
	v_mfma_f32_16x16x32_bf16 v[42:45], v[178:181], v[186:189], v[42:45]
	v_mfma_f32_16x16x32_bf16 v[62:65], v[156:159], v[194:197], v[62:65]
	v_mfma_f32_16x16x32_bf16 v[66:69], v[178:181], v[194:197], v[66:69]
	v_mfma_f32_16x16x32_bf16 v[82:85], v[156:159], v[202:205], v[82:85]
	v_mfma_f32_16x16x32_bf16 v[90:93], v[178:181], v[202:205], v[90:93]
	v_mfma_f32_16x16x32_bf16 v[106:109], v[156:159], v[210:213], v[106:109]
	v_mfma_f32_16x16x32_bf16 v[114:117], v[178:181], v[210:213], v[114:117]
	s_barrier
	ds_read_b128 v[182:185], v174 offset:49152
	ds_read_b128 v[186:189], v174 offset:50176
	ds_read_b128 v[190:193], v174 offset:51200
	ds_read_b128 v[194:197], v174 offset:52224
	ds_read_b128 v[198:201], v174 offset:53248
	ds_read_b128 v[202:205], v174 offset:54272
	ds_read_b128 v[206:209], v174 offset:55296
	ds_read_b128 v[210:213], v174 offset:56320
	s_add_u32 s28, s23, 0x180
	s_addc_u32 s29, s24, 0
	s_mov_b32 s25, m0
	s_mov_b32 m0, s92
	s_nop 2
	global_load_lds_dwordx4 v166, s[28:29]
	s_mov_b32 m0, s25
	s_nop 0
	s_mov_b32 s25, m0
	s_mov_b32 m0, s93
	s_nop 2
	global_load_lds_dwordx4 v168, s[28:29]
	s_mov_b32 m0, s25
	s_add_u32 s28, s23, 0x40180
	s_addc_u32 s29, s24, 0
	s_mov_b32 s23, m0
	s_mov_b32 m0, s96
	s_nop 2
	global_load_lds_dwordx4 v166, s[28:29]
	s_mov_b32 m0, s23
	s_nop 0
	s_mov_b32 s23, m0
	s_mov_b32 m0, s97
	s_nop 2
	global_load_lds_dwordx4 v168, s[28:29]
	s_mov_b32 m0, s23
	s_nop 0
	s_mov_b32 s23, m0
	s_mov_b32 m0, s94
	s_nop 2
	global_load_lds_dwordx4 v165, s[58:59]
	s_mov_b32 m0, s23
	s_nop 0
	s_mov_b32 s23, m0
	s_mov_b32 m0, s95
	s_nop 2
	global_load_lds_dwordx4 v167, s[58:59]
	s_mov_b32 m0, s23
	s_waitcnt vmcnt(8)
	s_waitcnt lgkmcnt(0)
	s_barrier
	v_mfma_f32_16x16x32_bf16 v[118:121], v[136:139], v[182:185], v[118:121]
	v_mfma_f32_16x16x32_bf16 v[126:129], v[144:147], v[182:185], v[126:129]
	v_mfma_f32_16x16x32_bf16 v[98:101], v[136:139], v[190:193], v[98:101]
	v_mfma_f32_16x16x32_bf16 v[86:89], v[144:147], v[190:193], v[86:89]
	v_mfma_f32_16x16x32_bf16 v[46:49], v[136:139], v[198:201], v[46:49]
	v_mfma_f32_16x16x32_bf16 v[34:37], v[144:147], v[198:201], v[34:37]
	v_mfma_f32_16x16x32_bf16 v[14:17], v[136:139], v[206:209], v[14:17]
	v_mfma_f32_16x16x32_bf16 v[10:13], v[144:147], v[206:209], v[10:13]
	v_mfma_f32_16x16x32_bf16 v[118:121], v[140:143], v[186:189], v[118:121]
	v_mfma_f32_16x16x32_bf16 v[126:129], v[148:151], v[186:189], v[126:129]
	v_mfma_f32_16x16x32_bf16 v[98:101], v[140:143], v[194:197], v[98:101]
	v_mfma_f32_16x16x32_bf16 v[86:89], v[148:151], v[194:197], v[86:89]
	v_mfma_f32_16x16x32_bf16 v[46:49], v[140:143], v[202:205], v[46:49]
	v_mfma_f32_16x16x32_bf16 v[34:37], v[148:151], v[202:205], v[34:37]
	v_mfma_f32_16x16x32_bf16 v[14:17], v[140:143], v[210:213], v[14:17]
	v_mfma_f32_16x16x32_bf16 v[10:13], v[148:151], v[210:213], v[10:13]
	v_mfma_f32_16x16x32_bf16 v[122:125], v[152:155], v[182:185], v[122:125]
	v_mfma_f32_16x16x32_bf16 v[110:113], v[160:163], v[182:185], v[110:113]
	v_mfma_f32_16x16x32_bf16 v[70:73], v[152:155], v[190:193], v[70:73]
	v_mfma_f32_16x16x32_bf16 v[58:61], v[160:163], v[190:193], v[58:61]
	v_mfma_f32_16x16x32_bf16 v[22:25], v[152:155], v[198:201], v[22:25]
	v_mfma_f32_16x16x32_bf16 v[18:21], v[160:163], v[198:201], v[18:21]
	v_mfma_f32_16x16x32_bf16 v[6:9], v[152:155], v[206:209], v[6:9]
	v_mfma_f32_16x16x32_bf16 v[2:5], v[160:163], v[206:209], v[2:5]
	v_mfma_f32_16x16x32_bf16 v[122:125], v[156:159], v[186:189], v[122:125]
	v_mfma_f32_16x16x32_bf16 v[110:113], v[178:181], v[186:189], v[110:113]
	v_mfma_f32_16x16x32_bf16 v[70:73], v[156:159], v[194:197], v[70:73]
	v_mfma_f32_16x16x32_bf16 v[58:61], v[178:181], v[194:197], v[58:61]
	v_mfma_f32_16x16x32_bf16 v[22:25], v[156:159], v[202:205], v[22:25]
	v_mfma_f32_16x16x32_bf16 v[18:21], v[178:181], v[202:205], v[18:21]
	v_mfma_f32_16x16x32_bf16 v[6:9], v[156:159], v[210:213], v[6:9]
	v_mfma_f32_16x16x32_bf16 v[2:5], v[178:181], v[210:213], v[2:5]
	s_barrier
	s_add_i32 s3, s3, 2
	s_add_u32 s56, s56, 0x100
	s_addc_u32 s57, s57, 0
	s_cmp_gt_u32 s3, 5
	s_cbranch_scc0 .LBB0_1046
	s_ashr_i32 s55, s54, 31
	s_lshl_b64 s[24:25], s[54:55], 19
	s_add_u32 s56, s69, s24
	s_addc_u32 s57, s76, s25
	s_ashr_i32 s23, s22, 31
	s_lshl_b64 s[24:25], s[22:23], 19
	s_add_u32 s58, s77, s24
	s_addc_u32 s59, s78, s25
	s_lshl_b32 s3, s60, 18
	s_lshl_b32 s23, s2, 8
	s_lshl_b32 s32, s2, 16
	s_add_i32 s2, s32, s3
	v_lshrrev_b32_e32 v214, 6, v0
	v_lshlrev_b32_e32 v214, 13, v214
	v_and_b32_e32 v215, 63, v0
	v_lshl_add_u32 v214, v215, 3, v214
	v_add_u32_e32 v134, s2, v214
	s_cmp_lg_u32 s37, 0
	s_cbranch_scc1 .Lmpf_have
	global_load_dwordx2 v[162:163], v134, s[14:15]
	global_load_dwordx2 v[178:179], v134, s[16:17]
	v_or_b32_e32 v136, 0x200, v134
	v_add_u32_e32 v137, 0x400, v134
	v_add_u32_e32 v138, 0x600, v134
	v_add_u32_e32 v139, 0x800, v134
	v_add_u32_e32 v140, 0xa00, v134
	v_add_u32_e32 v141, 0xc00, v134
	v_add_u32_e32 v161, 0xe00, v134
	global_load_dwordx2 v[180:181], v136, s[14:15]
	global_load_dwordx2 v[182:183], v136, s[16:17]
	global_load_dwordx2 v[158:159], v137, s[14:15]
	global_load_dwordx2 v[156:157], v137, s[16:17]
	global_load_dwordx2 v[154:155], v138, s[14:15]
	global_load_dwordx2 v[152:153], v138, s[16:17]
	global_load_dwordx2 v[150:151], v139, s[14:15]
	global_load_dwordx2 v[148:149], v139, s[16:17]
	global_load_dwordx2 v[146:147], v140, s[14:15]
	global_load_dwordx2 v[144:145], v140, s[16:17]
	global_load_dwordx2 v[142:143], v141, s[14:15]
	s_nop 0
	global_load_dwordx2 v[140:141], v141, s[16:17]
	s_nop 0
	global_load_dwordx2 v[138:139], v161, s[14:15]
	global_load_dwordx2 v[136:137], v161, s[16:17]
	s_branch .Lmpf_join

.LBB0_1048:
	ds_read_b128 v[136:139], v172
	ds_read_b128 v[140:143], v172 offset:1024
	ds_read_b128 v[144:147], v172 offset:2048
	ds_read_b128 v[148:151], v172 offset:3072
	ds_read_b128 v[152:155], v173
	ds_read_b128 v[156:159], v173 offset:1024
	ds_read_b128 v[160:163], v173 offset:2048
	ds_read_b128 v[178:181], v173 offset:3072
	s_cmp_eq_u32 s33, 12
	s_cselect_b32 s66, s3, s28
	s_cselect_b32 s67, s2, s29
	s_cselect_b32 s64, s25, s30
	s_cselect_b32 s65, s24, s31
	s_add_u32 s62, s66, 0x80
	s_addc_u32 s63, s67, 0
	ds_read_b128 v[182:185], v174
	ds_read_b128 v[186:189], v174 offset:1024
	ds_read_b128 v[190:193], v174 offset:2048
	ds_read_b128 v[194:197], v174 offset:3072
	ds_read_b128 v[198:201], v174 offset:4096
	ds_read_b128 v[202:205], v174 offset:5120
	ds_read_b128 v[206:209], v174 offset:6144
	ds_read_b128 v[210:213], v174 offset:7168
	s_add_u32 s36, s28, 0x3ff80
	s_addc_u32 s37, s29, 0
	s_mov_b32 s52, m0
	s_mov_b32 m0, s26
	s_nop 2
	global_load_lds_dwordx4 v165, s[36:37]
	s_mov_b32 m0, s52
	s_nop 0
	s_mov_b32 s52, m0
	s_mov_b32 m0, s27
	s_nop 2
	global_load_lds_dwordx4 v167, s[36:37]
	s_mov_b32 m0, s52
	s_waitcnt vmcnt(8)
	s_waitcnt lgkmcnt(0)
	s_barrier
	v_mfma_f32_16x16x32_bf16 v[26:29], v[136:139], v[182:185], v[26:29]
	v_mfma_f32_16x16x32_bf16 v[30:33], v[144:147], v[182:185], v[30:33]
	v_mfma_f32_16x16x32_bf16 v[50:53], v[136:139], v[190:193], v[50:53]
	v_mfma_f32_16x16x32_bf16 v[54:57], v[144:147], v[190:193], v[54:57]
	v_mfma_f32_16x16x32_bf16 v[74:77], v[136:139], v[198:201], v[74:77]
	v_mfma_f32_16x16x32_bf16 v[78:81], v[144:147], v[198:201], v[78:81]
	v_mfma_f32_16x16x32_bf16 v[94:97], v[136:139], v[206:209], v[94:97]
	v_mfma_f32_16x16x32_bf16 v[102:105], v[144:147], v[206:209], v[102:105]
	v_mfma_f32_16x16x32_bf16 v[26:29], v[140:143], v[186:189], v[26:29]
	v_mfma_f32_16x16x32_bf16 v[30:33], v[148:151], v[186:189], v[30:33]
	v_mfma_f32_16x16x32_bf16 v[50:53], v[140:143], v[194:197], v[50:53]
	v_mfma_f32_16x16x32_bf16 v[54:57], v[148:151], v[194:197], v[54:57]
	v_mfma_f32_16x16x32_bf16 v[74:77], v[140:143], v[202:205], v[74:77]
	v_mfma_f32_16x16x32_bf16 v[78:81], v[148:151], v[202:205], v[78:81]
	v_mfma_f32_16x16x32_bf16 v[94:97], v[140:143], v[210:213], v[94:97]
	v_mfma_f32_16x16x32_bf16 v[102:105], v[148:151], v[210:213], v[102:105]
	v_mfma_f32_16x16x32_bf16 v[38:41], v[152:155], v[182:185], v[38:41]
	v_mfma_f32_16x16x32_bf16 v[42:45], v[160:163], v[182:185], v[42:45]
	v_mfma_f32_16x16x32_bf16 v[62:65], v[152:155], v[190:193], v[62:65]
	v_mfma_f32_16x16x32_bf16 v[66:69], v[160:163], v[190:193], v[66:69]
	v_mfma_f32_16x16x32_bf16 v[82:85], v[152:155], v[198:201], v[82:85]
	v_mfma_f32_16x16x32_bf16 v[90:93], v[160:163], v[198:201], v[90:93]
	v_mfma_f32_16x16x32_bf16 v[106:109], v[152:155], v[206:209], v[106:109]
	v_mfma_f32_16x16x32_bf16 v[114:117], v[160:163], v[206:209], v[114:117]
	v_mfma_f32_16x16x32_bf16 v[38:41], v[156:159], v[186:189], v[38:41]
	v_mfma_f32_16x16x32_bf16 v[42:45], v[178:181], v[186:189], v[42:45]
	v_mfma_f32_16x16x32_bf16 v[62:65], v[156:159], v[194:197], v[62:65]
	v_mfma_f32_16x16x32_bf16 v[66:69], v[178:181], v[194:197], v[66:69]
	v_mfma_f32_16x16x32_bf16 v[82:85], v[156:159], v[202:205], v[82:85]
	v_mfma_f32_16x16x32_bf16 v[90:93], v[178:181], v[202:205], v[90:93]
	v_mfma_f32_16x16x32_bf16 v[106:109], v[156:159], v[210:213], v[106:109]
	v_mfma_f32_16x16x32_bf16 v[114:117], v[178:181], v[210:213], v[114:117]
	s_barrier
	ds_read_b128 v[182:185], v174 offset:16384
	ds_read_b128 v[186:189], v174 offset:17408
	ds_read_b128 v[190:193], v174 offset:18432
	ds_read_b128 v[194:197], v174 offset:19456
	ds_read_b128 v[198:201], v174 offset:20480
	ds_read_b128 v[202:205], v174 offset:21504
	ds_read_b128 v[206:209], v174 offset:22528
	ds_read_b128 v[210:213], v174 offset:23552
	s_mov_b32 s36, m0
	s_mov_b32 m0, s80
	s_nop 2
	global_load_lds_dwordx4 v166, s[64:65]
	s_mov_b32 m0, s36
	s_nop 0
	s_mov_b32 s36, m0
	s_mov_b32 m0, s81
	s_nop 2
	global_load_lds_dwordx4 v168, s[64:65]
	s_mov_b32 m0, s36
	s_add_u32 s36, s64, 0x40000
	s_addc_u32 s37, s65, 0
	s_mov_b32 s52, m0
	s_mov_b32 m0, s82
	s_nop 2
	global_load_lds_dwordx4 v166, s[36:37]
	s_mov_b32 m0, s52
	s_nop 0
	s_mov_b32 s52, m0
	s_mov_b32 m0, s83
	s_nop 2
	global_load_lds_dwordx4 v168, s[36:37]
	s_mov_b32 m0, s52
	s_mov_b32 s36, m0
	s_mov_b32 m0, s79
	s_nop 2
	global_load_lds_dwordx4 v165, s[66:67]
	s_mov_b32 m0, s36
	s_nop 0
	s_mov_b32 s36, m0
	s_mov_b32 m0, s84
	s_nop 2
	global_load_lds_dwordx4 v167, s[66:67]
	s_mov_b32 m0, s36
	s_waitcnt vmcnt(8)
	s_waitcnt lgkmcnt(0)
	s_barrier
	v_mfma_f32_16x16x32_bf16 v[118:121], v[136:139], v[182:185], v[118:121]
	v_mfma_f32_16x16x32_bf16 v[126:129], v[144:147], v[182:185], v[126:129]
	v_mfma_f32_16x16x32_bf16 v[98:101], v[136:139], v[190:193], v[98:101]
	v_mfma_f32_16x16x32_bf16 v[86:89], v[144:147], v[190:193], v[86:89]
	v_mfma_f32_16x16x32_bf16 v[46:49], v[136:139], v[198:201], v[46:49]
	v_mfma_f32_16x16x32_bf16 v[34:37], v[144:147], v[198:201], v[34:37]
	v_mfma_f32_16x16x32_bf16 v[14:17], v[136:139], v[206:209], v[14:17]
	v_mfma_f32_16x16x32_bf16 v[10:13], v[144:147], v[206:209], v[10:13]
	v_mfma_f32_16x16x32_bf16 v[118:121], v[140:143], v[186:189], v[118:121]
	v_mfma_f32_16x16x32_bf16 v[126:129], v[148:151], v[186:189], v[126:129]
	v_mfma_f32_16x16x32_bf16 v[98:101], v[140:143], v[194:197], v[98:101]
	v_mfma_f32_16x16x32_bf16 v[86:89], v[148:151], v[194:197], v[86:89]
	v_mfma_f32_16x16x32_bf16 v[46:49], v[140:143], v[202:205], v[46:49]
	v_mfma_f32_16x16x32_bf16 v[34:37], v[148:151], v[202:205], v[34:37]
	v_mfma_f32_16x16x32_bf16 v[14:17], v[140:143], v[210:213], v[14:17]
	v_mfma_f32_16x16x32_bf16 v[10:13], v[148:151], v[210:213], v[10:13]
	v_mfma_f32_16x16x32_bf16 v[122:125], v[152:155], v[182:185], v[122:125]
	v_mfma_f32_16x16x32_bf16 v[110:113], v[160:163], v[182:185], v[110:113]
	v_mfma_f32_16x16x32_bf16 v[70:73], v[152:155], v[190:193], v[70:73]
	v_mfma_f32_16x16x32_bf16 v[58:61], v[160:163], v[190:193], v[58:61]
	v_mfma_f32_16x16x32_bf16 v[22:25], v[152:155], v[198:201], v[22:25]
	v_mfma_f32_16x16x32_bf16 v[18:21], v[160:163], v[198:201], v[18:21]
	v_mfma_f32_16x16x32_bf16 v[6:9], v[152:155], v[206:209], v[6:9]
	v_mfma_f32_16x16x32_bf16 v[2:5], v[160:163], v[206:209], v[2:5]
	v_mfma_f32_16x16x32_bf16 v[122:125], v[156:159], v[186:189], v[122:125]
	v_mfma_f32_16x16x32_bf16 v[110:113], v[178:181], v[186:189], v[110:113]
	v_mfma_f32_16x16x32_bf16 v[70:73], v[156:159], v[194:197], v[70:73]
	v_mfma_f32_16x16x32_bf16 v[58:61], v[178:181], v[194:197], v[58:61]
	v_mfma_f32_16x16x32_bf16 v[22:25], v[156:159], v[202:205], v[22:25]
	v_mfma_f32_16x16x32_bf16 v[18:21], v[178:181], v[202:205], v[18:21]
	v_mfma_f32_16x16x32_bf16 v[6:9], v[156:159], v[210:213], v[6:9]
	v_mfma_f32_16x16x32_bf16 v[2:5], v[178:181], v[210:213], v[2:5]
	s_barrier
	ds_read_b128 v[136:139], v175
	ds_read_b128 v[140:143], v175 offset:1024
	ds_read_b128 v[144:147], v175 offset:2048
	ds_read_b128 v[148:151], v175 offset:3072
	ds_read_b128 v[152:155], v176
	ds_read_b128 v[156:159], v176 offset:1024
	ds_read_b128 v[160:163], v176 offset:2048
	ds_read_b128 v[178:181], v176 offset:3072
	ds_read_b128 v[182:185], v174 offset:32768
	ds_read_b128 v[186:189], v174 offset:33792
	ds_read_b128 v[190:193], v174 offset:34816
	ds_read_b128 v[194:197], v174 offset:35840
	ds_read_b128 v[198:201], v174 offset:36864
	ds_read_b128 v[202:205], v174 offset:37888
	ds_read_b128 v[206:209], v174 offset:38912
	ds_read_b128 v[210:213], v174 offset:39936
	s_add_u32 s36, s66, 0x40000
	s_addc_u32 s37, s67, 0
	s_mov_b32 s52, m0
	s_mov_b32 m0, s85
	s_nop 2
	global_load_lds_dwordx4 v165, s[36:37]
	s_mov_b32 m0, s52
	s_nop 0
	s_mov_b32 s52, m0
	s_mov_b32 m0, s86
	s_nop 2
	global_load_lds_dwordx4 v167, s[36:37]
	s_mov_b32 m0, s52
	s_waitcnt vmcnt(8)
	s_waitcnt lgkmcnt(0)
	s_barrier
	v_mfma_f32_16x16x32_bf16 v[26:29], v[136:139], v[182:185], v[26:29]
	v_mfma_f32_16x16x32_bf16 v[30:33], v[144:147], v[182:185], v[30:33]
	v_mfma_f32_16x16x32_bf16 v[50:53], v[136:139], v[190:193], v[50:53]
	v_mfma_f32_16x16x32_bf16 v[54:57], v[144:147], v[190:193], v[54:57]
	v_mfma_f32_16x16x32_bf16 v[74:77], v[136:139], v[198:201], v[74:77]
	v_mfma_f32_16x16x32_bf16 v[78:81], v[144:147], v[198:201], v[78:81]
	v_mfma_f32_16x16x32_bf16 v[94:97], v[136:139], v[206:209], v[94:97]
	v_mfma_f32_16x16x32_bf16 v[102:105], v[144:147], v[206:209], v[102:105]
	v_mfma_f32_16x16x32_bf16 v[26:29], v[140:143], v[186:189], v[26:29]
	v_mfma_f32_16x16x32_bf16 v[30:33], v[148:151], v[186:189], v[30:33]
	v_mfma_f32_16x16x32_bf16 v[50:53], v[140:143], v[194:197], v[50:53]
	v_mfma_f32_16x16x32_bf16 v[54:57], v[148:151], v[194:197], v[54:57]
	v_mfma_f32_16x16x32_bf16 v[74:77], v[140:143], v[202:205], v[74:77]
	v_mfma_f32_16x16x32_bf16 v[78:81], v[148:151], v[202:205], v[78:81]
	v_mfma_f32_16x16x32_bf16 v[94:97], v[140:143], v[210:213], v[94:97]
	v_mfma_f32_16x16x32_bf16 v[102:105], v[148:151], v[210:213], v[102:105]
	v_mfma_f32_16x16x32_bf16 v[38:41], v[152:155], v[182:185], v[38:41]
	v_mfma_f32_16x16x32_bf16 v[42:45], v[160:163], v[182:185], v[42:45]
	v_mfma_f32_16x16x32_bf16 v[62:65], v[152:155], v[190:193], v[62:65]
	v_mfma_f32_16x16x32_bf16 v[66:69], v[160:163], v[190:193], v[66:69]
	v_mfma_f32_16x16x32_bf16 v[82:85], v[152:155], v[198:201], v[82:85]
	v_mfma_f32_16x16x32_bf16 v[90:93], v[160:163], v[198:201], v[90:93]
	v_mfma_f32_16x16x32_bf16 v[106:109], v[152:155], v[206:209], v[106:109]
	v_mfma_f32_16x16x32_bf16 v[114:117], v[160:163], v[206:209], v[114:117]
	v_mfma_f32_16x16x32_bf16 v[38:41], v[156:159], v[186:189], v[38:41]
	v_mfma_f32_16x16x32_bf16 v[42:45], v[178:181], v[186:189], v[42:45]
	v_mfma_f32_16x16x32_bf16 v[62:65], v[156:159], v[194:197], v[62:65]
	v_mfma_f32_16x16x32_bf16 v[66:69], v[178:181], v[194:197], v[66:69]
	v_mfma_f32_16x16x32_bf16 v[82:85], v[156:159], v[202:205], v[82:85]
	v_mfma_f32_16x16x32_bf16 v[90:93], v[178:181], v[202:205], v[90:93]
	v_mfma_f32_16x16x32_bf16 v[106:109], v[156:159], v[210:213], v[106:109]
	v_mfma_f32_16x16x32_bf16 v[114:117], v[178:181], v[210:213], v[114:117]
	s_barrier
	ds_read_b128 v[182:185], v174 offset:49152
	ds_read_b128 v[186:189], v174 offset:50176
	ds_read_b128 v[190:193], v174 offset:51200
	ds_read_b128 v[194:197], v174 offset:52224
	ds_read_b128 v[198:201], v174 offset:53248
	ds_read_b128 v[202:205], v174 offset:54272
	ds_read_b128 v[206:209], v174 offset:55296
	ds_read_b128 v[210:213], v174 offset:56320
	s_add_u32 s36, s64, 0x80
	s_addc_u32 s37, s65, 0
	s_mov_b32 s52, m0
	s_mov_b32 m0, s92
	s_nop 2
	global_load_lds_dwordx4 v166, s[36:37]
	s_mov_b32 m0, s52
	s_nop 0
	s_mov_b32 s52, m0
	s_mov_b32 m0, s93
	s_nop 2
	global_load_lds_dwordx4 v168, s[36:37]
	s_mov_b32 m0, s52
	s_add_u32 s36, s64, 0x40080
	s_addc_u32 s37, s65, 0
	s_mov_b32 s52, m0
	s_mov_b32 m0, s96
	s_nop 2
	global_load_lds_dwordx4 v166, s[36:37]
	s_mov_b32 m0, s52
	s_nop 0
	s_mov_b32 s52, m0
	s_mov_b32 m0, s97
	s_nop 2
	global_load_lds_dwordx4 v168, s[36:37]
	s_mov_b32 m0, s52
	s_mov_b32 s36, m0
	s_mov_b32 m0, s94
	s_nop 2
	global_load_lds_dwordx4 v165, s[62:63]
	s_mov_b32 m0, s36
	s_nop 0
	s_mov_b32 s36, m0
	s_mov_b32 m0, s95
	s_nop 2
	global_load_lds_dwordx4 v167, s[62:63]
	s_mov_b32 m0, s36
	s_waitcnt vmcnt(8)
	s_waitcnt lgkmcnt(0)
	s_barrier
	v_mfma_f32_16x16x32_bf16 v[118:121], v[136:139], v[182:185], v[118:121]
	v_mfma_f32_16x16x32_bf16 v[126:129], v[144:147], v[182:185], v[126:129]
	v_mfma_f32_16x16x32_bf16 v[98:101], v[136:139], v[190:193], v[98:101]
	v_mfma_f32_16x16x32_bf16 v[86:89], v[144:147], v[190:193], v[86:89]
	v_mfma_f32_16x16x32_bf16 v[46:49], v[136:139], v[198:201], v[46:49]
	v_mfma_f32_16x16x32_bf16 v[34:37], v[144:147], v[198:201], v[34:37]
	v_mfma_f32_16x16x32_bf16 v[14:17], v[136:139], v[206:209], v[14:17]
	v_mfma_f32_16x16x32_bf16 v[10:13], v[144:147], v[206:209], v[10:13]
	v_mfma_f32_16x16x32_bf16 v[118:121], v[140:143], v[186:189], v[118:121]
	v_mfma_f32_16x16x32_bf16 v[126:129], v[148:151], v[186:189], v[126:129]
	v_mfma_f32_16x16x32_bf16 v[98:101], v[140:143], v[194:197], v[98:101]
	v_mfma_f32_16x16x32_bf16 v[86:89], v[148:151], v[194:197], v[86:89]
	v_mfma_f32_16x16x32_bf16 v[46:49], v[140:143], v[202:205], v[46:49]
	v_mfma_f32_16x16x32_bf16 v[34:37], v[148:151], v[202:205], v[34:37]
	v_mfma_f32_16x16x32_bf16 v[14:17], v[140:143], v[210:213], v[14:17]
	v_mfma_f32_16x16x32_bf16 v[10:13], v[148:151], v[210:213], v[10:13]
	v_mfma_f32_16x16x32_bf16 v[122:125], v[152:155], v[182:185], v[122:125]
	v_mfma_f32_16x16x32_bf16 v[110:113], v[160:163], v[182:185], v[110:113]
	v_mfma_f32_16x16x32_bf16 v[70:73], v[152:155], v[190:193], v[70:73]
	v_mfma_f32_16x16x32_bf16 v[58:61], v[160:163], v[190:193], v[58:61]
	v_mfma_f32_16x16x32_bf16 v[22:25], v[152:155], v[198:201], v[22:25]
	v_mfma_f32_16x16x32_bf16 v[18:21], v[160:163], v[198:201], v[18:21]
	v_mfma_f32_16x16x32_bf16 v[6:9], v[152:155], v[206:209], v[6:9]
	v_mfma_f32_16x16x32_bf16 v[2:5], v[160:163], v[206:209], v[2:5]
	v_mfma_f32_16x16x32_bf16 v[122:125], v[156:159], v[186:189], v[122:125]
	v_mfma_f32_16x16x32_bf16 v[110:113], v[178:181], v[186:189], v[110:113]
	v_mfma_f32_16x16x32_bf16 v[70:73], v[156:159], v[194:197], v[70:73]
	v_mfma_f32_16x16x32_bf16 v[58:61], v[178:181], v[194:197], v[58:61]
	v_mfma_f32_16x16x32_bf16 v[22:25], v[156:159], v[202:205], v[22:25]
	v_mfma_f32_16x16x32_bf16 v[18:21], v[178:181], v[202:205], v[18:21]
	v_mfma_f32_16x16x32_bf16 v[6:9], v[156:159], v[210:213], v[6:9]
	v_mfma_f32_16x16x32_bf16 v[2:5], v[178:181], v[210:213], v[2:5]
	s_barrier
	s_add_i32 s33, s33, 2
	s_add_u32 s28, s28, 0x100
	s_addc_u32 s29, s29, 0
	s_add_u32 s30, s30, 0x100
	s_addc_u32 s31, s31, 0
	s_cmp_lt_u32 s33, 14
	s_cbranch_scc1 .LBB0_1048
	s_and_b64 vcc, exec, s[20:21]
	s_cbranch_vccz .LBB0_1051
	s_barrier

.Lpeel1440:
	ds_read_b128 v[130:133], v234
	ds_read_b128 v[134:137], v234 offset:1024
	ds_read_b128 v[138:141], v234 offset:2048
	ds_read_b128 v[142:145], v234 offset:3072
	ds_read_b128 v[146:149], v235
	ds_read_b128 v[150:153], v235 offset:1024
	ds_read_b128 v[154:157], v235 offset:2048
	ds_read_b128 v[158:161], v235 offset:3072
	s_add_u32 s60, s58, 0x100
	s_addc_u32 s61, s59, 0
	s_cmp_eq_u32 s87, 12
	s_cselect_b32 s66, s33, s60
	s_cselect_b32 s67, s21, s61
	s_cselect_b32 s64, s84, s85
	s_cselect_b32 s65, s19, s86
	s_add_u32 s62, s66, 0x80
	s_addc_u32 s63, s67, 0
	ds_read_b128 v[162:165], v236
	ds_read_b128 v[166:169], v236 offset:1024
	ds_read_b128 v[170:173], v236 offset:2048
	ds_read_b128 v[174:177], v236 offset:3072
	ds_read_b128 v[178:181], v236 offset:4096
	ds_read_b128 v[182:185], v236 offset:5120
	ds_read_b128 v[186:189], v236 offset:6144
	ds_read_b128 v[190:193], v236 offset:7168
	s_add_u32 s58, s58, 0x40080
	s_addc_u32 s59, s59, 0
	s_mov_b32 s88, m0
	s_mov_b32 m0, s80
	s_nop 2
	global_load_lds_dwordx4 v228, s[58:59]
	s_mov_b32 m0, s88
	s_nop 0
	s_mov_b32 s88, m0
	s_mov_b32 m0, s81
	s_nop 2
	global_load_lds_dwordx4 v230, s[58:59]
	s_mov_b32 m0, s88
	s_waitcnt vmcnt(8)
	s_waitcnt lgkmcnt(0)
	s_barrier
	v_mfma_f32_16x16x32_bf16 v[126:129], v[130:133], v[162:165], 0
	v_mfma_f32_16x16x32_bf16 v[122:125], v[138:141], v[162:165], 0
	v_mfma_f32_16x16x32_bf16 v[114:117], v[130:133], v[170:173], 0
	v_mfma_f32_16x16x32_bf16 v[106:109], v[138:141], v[170:173], 0
	v_mfma_f32_16x16x32_bf16 v[94:97], v[130:133], v[178:181], 0
	v_mfma_f32_16x16x32_bf16 v[90:93], v[138:141], v[178:181], 0
	v_mfma_f32_16x16x32_bf16 v[86:89], v[130:133], v[186:189], 0
	v_mfma_f32_16x16x32_bf16 v[78:81], v[138:141], v[186:189], 0
	v_mfma_f32_16x16x32_bf16 v[126:129], v[134:137], v[166:169], v[126:129]
	v_mfma_f32_16x16x32_bf16 v[122:125], v[142:145], v[166:169], v[122:125]
	v_mfma_f32_16x16x32_bf16 v[114:117], v[134:137], v[174:177], v[114:117]
	v_mfma_f32_16x16x32_bf16 v[106:109], v[142:145], v[174:177], v[106:109]
	v_mfma_f32_16x16x32_bf16 v[94:97], v[134:137], v[182:185], v[94:97]
	v_mfma_f32_16x16x32_bf16 v[90:93], v[142:145], v[182:185], v[90:93]
	v_mfma_f32_16x16x32_bf16 v[86:89], v[134:137], v[190:193], v[86:89]
	v_mfma_f32_16x16x32_bf16 v[78:81], v[142:145], v[190:193], v[78:81]
	v_mfma_f32_16x16x32_bf16 v[118:121], v[146:149], v[162:165], 0
	v_mfma_f32_16x16x32_bf16 v[110:113], v[154:157], v[162:165], 0
	v_mfma_f32_16x16x32_bf16 v[102:105], v[146:149], v[170:173], 0
	v_mfma_f32_16x16x32_bf16 v[98:101], v[154:157], v[170:173], 0
	v_mfma_f32_16x16x32_bf16 v[82:85], v[146:149], v[178:181], 0
	v_mfma_f32_16x16x32_bf16 v[74:77], v[154:157], v[178:181], 0
	v_mfma_f32_16x16x32_bf16 v[70:73], v[146:149], v[186:189], 0
	v_mfma_f32_16x16x32_bf16 v[66:69], v[154:157], v[186:189], 0
	v_mfma_f32_16x16x32_bf16 v[118:121], v[150:153], v[166:169], v[118:121]
	v_mfma_f32_16x16x32_bf16 v[110:113], v[158:161], v[166:169], v[110:113]
	v_mfma_f32_16x16x32_bf16 v[102:105], v[150:153], v[174:177], v[102:105]
	v_mfma_f32_16x16x32_bf16 v[98:101], v[158:161], v[174:177], v[98:101]
	v_mfma_f32_16x16x32_bf16 v[82:85], v[150:153], v[182:185], v[82:85]
	v_mfma_f32_16x16x32_bf16 v[74:77], v[158:161], v[182:185], v[74:77]
	v_mfma_f32_16x16x32_bf16 v[70:73], v[150:153], v[190:193], v[70:73]
	v_mfma_f32_16x16x32_bf16 v[66:69], v[158:161], v[190:193], v[66:69]
	s_barrier
	ds_read_b128 v[162:165], v236 offset:16384
	ds_read_b128 v[166:169], v236 offset:17408
	ds_read_b128 v[170:173], v236 offset:18432
	ds_read_b128 v[174:177], v236 offset:19456
	ds_read_b128 v[178:181], v236 offset:20480
	ds_read_b128 v[182:185], v236 offset:21504
	ds_read_b128 v[186:189], v236 offset:22528
	ds_read_b128 v[190:193], v236 offset:23552
	s_mov_b32 s58, m0
	s_mov_b32 m0, s30
	s_nop 2
	global_load_lds_dwordx4 v229, s[64:65]
	s_mov_b32 m0, s58
	s_nop 0
	s_mov_b32 s58, m0
	s_mov_b32 m0, s31
	s_nop 2
	global_load_lds_dwordx4 v231, s[64:65]
	s_mov_b32 m0, s58
	s_add_u32 s58, s64, 0x40000
	s_addc_u32 s59, s65, 0
	s_mov_b32 s88, m0
	s_mov_b32 m0, s34
	s_nop 2
	global_load_lds_dwordx4 v229, s[58:59]
	s_mov_b32 m0, s88
	s_nop 0
	s_mov_b32 s88, m0
	s_mov_b32 m0, s35
	s_nop 2
	global_load_lds_dwordx4 v231, s[58:59]
	s_mov_b32 m0, s88
	s_mov_b32 s58, m0
	s_mov_b32 m0, s28
	s_nop 2
	global_load_lds_dwordx4 v228, s[66:67]
	s_mov_b32 m0, s58
	s_nop 0
	s_mov_b32 s58, m0
	s_mov_b32 m0, s36
	s_nop 2
	global_load_lds_dwordx4 v230, s[66:67]
	s_mov_b32 m0, s58
	s_waitcnt vmcnt(8)
	s_waitcnt lgkmcnt(0)
	s_barrier
	v_mfma_f32_16x16x32_bf16 v[62:65], v[130:133], v[162:165], 0
	v_mfma_f32_16x16x32_bf16 v[58:61], v[138:141], v[162:165], 0
	v_mfma_f32_16x16x32_bf16 v[54:57], v[130:133], v[170:173], 0
	v_mfma_f32_16x16x32_bf16 v[46:49], v[138:141], v[170:173], 0
	v_mfma_f32_16x16x32_bf16 v[38:41], v[130:133], v[178:181], 0
	v_mfma_f32_16x16x32_bf16 v[30:33], v[138:141], v[178:181], 0
	v_mfma_f32_16x16x32_bf16 v[22:25], v[130:133], v[186:189], 0
	v_mfma_f32_16x16x32_bf16 v[14:17], v[138:141], v[186:189], 0
	v_mfma_f32_16x16x32_bf16 v[62:65], v[134:137], v[166:169], v[62:65]
	v_mfma_f32_16x16x32_bf16 v[58:61], v[142:145], v[166:169], v[58:61]
	v_mfma_f32_16x16x32_bf16 v[54:57], v[134:137], v[174:177], v[54:57]
	v_mfma_f32_16x16x32_bf16 v[46:49], v[142:145], v[174:177], v[46:49]
	v_mfma_f32_16x16x32_bf16 v[38:41], v[134:137], v[182:185], v[38:41]
	v_mfma_f32_16x16x32_bf16 v[30:33], v[142:145], v[182:185], v[30:33]
	v_mfma_f32_16x16x32_bf16 v[22:25], v[134:137], v[190:193], v[22:25]
	v_mfma_f32_16x16x32_bf16 v[14:17], v[142:145], v[190:193], v[14:17]
	v_mfma_f32_16x16x32_bf16 v[50:53], v[146:149], v[162:165], 0
	v_mfma_f32_16x16x32_bf16 v[42:45], v[154:157], v[162:165], 0
	v_mfma_f32_16x16x32_bf16 v[34:37], v[146:149], v[170:173], 0
	v_mfma_f32_16x16x32_bf16 v[26:29], v[154:157], v[170:173], 0
	v_mfma_f32_16x16x32_bf16 v[18:21], v[146:149], v[178:181], 0
	v_mfma_f32_16x16x32_bf16 v[10:13], v[154:157], v[178:181], 0
	v_mfma_f32_16x16x32_bf16 v[6:9], v[146:149], v[186:189], 0
	v_mfma_f32_16x16x32_bf16 v[2:5], v[154:157], v[186:189], 0
	v_mfma_f32_16x16x32_bf16 v[50:53], v[150:153], v[166:169], v[50:53]
	v_mfma_f32_16x16x32_bf16 v[42:45], v[158:161], v[166:169], v[42:45]
	v_mfma_f32_16x16x32_bf16 v[34:37], v[150:153], v[174:177], v[34:37]
	v_mfma_f32_16x16x32_bf16 v[26:29], v[158:161], v[174:177], v[26:29]
	v_mfma_f32_16x16x32_bf16 v[18:21], v[150:153], v[182:185], v[18:21]
	v_mfma_f32_16x16x32_bf16 v[10:13], v[158:161], v[182:185], v[10:13]
	v_mfma_f32_16x16x32_bf16 v[6:9], v[150:153], v[190:193], v[6:9]
	v_mfma_f32_16x16x32_bf16 v[2:5], v[158:161], v[190:193], v[2:5]
	s_barrier
	s_branch .Lmid1440
.LBB0_1440:
	ds_read_b128 v[130:133], v234
	ds_read_b128 v[134:137], v234 offset:1024
	ds_read_b128 v[138:141], v234 offset:2048
	ds_read_b128 v[142:145], v234 offset:3072
	ds_read_b128 v[146:149], v235
	ds_read_b128 v[150:153], v235 offset:1024
	ds_read_b128 v[154:157], v235 offset:2048
	ds_read_b128 v[158:161], v235 offset:3072
	s_add_u32 s60, s58, 0x100
	s_addc_u32 s61, s59, 0
	s_cmp_eq_u32 s87, 12
	s_cselect_b32 s66, s33, s60
	s_cselect_b32 s67, s21, s61
	s_cselect_b32 s64, s84, s85
	s_cselect_b32 s65, s19, s86
	s_add_u32 s62, s66, 0x80
	s_addc_u32 s63, s67, 0
	ds_read_b128 v[162:165], v236
	ds_read_b128 v[166:169], v236 offset:1024
	ds_read_b128 v[170:173], v236 offset:2048
	ds_read_b128 v[174:177], v236 offset:3072
	ds_read_b128 v[178:181], v236 offset:4096
	ds_read_b128 v[182:185], v236 offset:5120
	ds_read_b128 v[186:189], v236 offset:6144
	ds_read_b128 v[190:193], v236 offset:7168
	s_add_u32 s58, s58, 0x40080
	s_addc_u32 s59, s59, 0
	s_mov_b32 s88, m0
	s_mov_b32 m0, s80
	s_nop 2
	global_load_lds_dwordx4 v228, s[58:59]
	s_mov_b32 m0, s88
	s_nop 0
	s_mov_b32 s88, m0
	s_mov_b32 m0, s81
	s_nop 2
	global_load_lds_dwordx4 v230, s[58:59]
	s_mov_b32 m0, s88
	s_waitcnt vmcnt(8)
	s_waitcnt lgkmcnt(0)
	s_barrier
	v_mfma_f32_16x16x32_bf16 v[126:129], v[130:133], v[162:165], v[126:129]
	v_mfma_f32_16x16x32_bf16 v[122:125], v[138:141], v[162:165], v[122:125]
	v_mfma_f32_16x16x32_bf16 v[114:117], v[130:133], v[170:173], v[114:117]
	v_mfma_f32_16x16x32_bf16 v[106:109], v[138:141], v[170:173], v[106:109]
	v_mfma_f32_16x16x32_bf16 v[94:97], v[130:133], v[178:181], v[94:97]
	v_mfma_f32_16x16x32_bf16 v[90:93], v[138:141], v[178:181], v[90:93]
	v_mfma_f32_16x16x32_bf16 v[86:89], v[130:133], v[186:189], v[86:89]
	v_mfma_f32_16x16x32_bf16 v[78:81], v[138:141], v[186:189], v[78:81]
	v_mfma_f32_16x16x32_bf16 v[126:129], v[134:137], v[166:169], v[126:129]
	v_mfma_f32_16x16x32_bf16 v[122:125], v[142:145], v[166:169], v[122:125]
	v_mfma_f32_16x16x32_bf16 v[114:117], v[134:137], v[174:177], v[114:117]
	v_mfma_f32_16x16x32_bf16 v[106:109], v[142:145], v[174:177], v[106:109]
	v_mfma_f32_16x16x32_bf16 v[94:97], v[134:137], v[182:185], v[94:97]
	v_mfma_f32_16x16x32_bf16 v[90:93], v[142:145], v[182:185], v[90:93]
	v_mfma_f32_16x16x32_bf16 v[86:89], v[134:137], v[190:193], v[86:89]
	v_mfma_f32_16x16x32_bf16 v[78:81], v[142:145], v[190:193], v[78:81]
	v_mfma_f32_16x16x32_bf16 v[118:121], v[146:149], v[162:165], v[118:121]
	v_mfma_f32_16x16x32_bf16 v[110:113], v[154:157], v[162:165], v[110:113]
	v_mfma_f32_16x16x32_bf16 v[102:105], v[146:149], v[170:173], v[102:105]
	v_mfma_f32_16x16x32_bf16 v[98:101], v[154:157], v[170:173], v[98:101]
	v_mfma_f32_16x16x32_bf16 v[82:85], v[146:149], v[178:181], v[82:85]
	v_mfma_f32_16x16x32_bf16 v[74:77], v[154:157], v[178:181], v[74:77]
	v_mfma_f32_16x16x32_bf16 v[70:73], v[146:149], v[186:189], v[70:73]
	v_mfma_f32_16x16x32_bf16 v[66:69], v[154:157], v[186:189], v[66:69]
	v_mfma_f32_16x16x32_bf16 v[118:121], v[150:153], v[166:169], v[118:121]
	v_mfma_f32_16x16x32_bf16 v[110:113], v[158:161], v[166:169], v[110:113]
	v_mfma_f32_16x16x32_bf16 v[102:105], v[150:153], v[174:177], v[102:105]
	v_mfma_f32_16x16x32_bf16 v[98:101], v[158:161], v[174:177], v[98:101]
	v_mfma_f32_16x16x32_bf16 v[82:85], v[150:153], v[182:185], v[82:85]
	v_mfma_f32_16x16x32_bf16 v[74:77], v[158:161], v[182:185], v[74:77]
	v_mfma_f32_16x16x32_bf16 v[70:73], v[150:153], v[190:193], v[70:73]
	v_mfma_f32_16x16x32_bf16 v[66:69], v[158:161], v[190:193], v[66:69]
	s_barrier
	ds_read_b128 v[162:165], v236 offset:16384
	ds_read_b128 v[166:169], v236 offset:17408
	ds_read_b128 v[170:173], v236 offset:18432
	ds_read_b128 v[174:177], v236 offset:19456
	ds_read_b128 v[178:181], v236 offset:20480
	ds_read_b128 v[182:185], v236 offset:21504
	ds_read_b128 v[186:189], v236 offset:22528
	ds_read_b128 v[190:193], v236 offset:23552
	s_mov_b32 s58, m0
	s_mov_b32 m0, s30
	s_nop 2
	global_load_lds_dwordx4 v229, s[64:65]
	s_mov_b32 m0, s58
	s_nop 0
	s_mov_b32 s58, m0
	s_mov_b32 m0, s31
	s_nop 2
	global_load_lds_dwordx4 v231, s[64:65]
	s_mov_b32 m0, s58
	s_add_u32 s58, s64, 0x40000
	s_addc_u32 s59, s65, 0
	s_mov_b32 s88, m0
	s_mov_b32 m0, s34
	s_nop 2
	global_load_lds_dwordx4 v229, s[58:59]
	s_mov_b32 m0, s88
	s_nop 0
	s_mov_b32 s88, m0
	s_mov_b32 m0, s35
	s_nop 2
	global_load_lds_dwordx4 v231, s[58:59]
	s_mov_b32 m0, s88
	s_mov_b32 s58, m0
	s_mov_b32 m0, s28
	s_nop 2
	global_load_lds_dwordx4 v228, s[66:67]
	s_mov_b32 m0, s58
	s_nop 0
	s_mov_b32 s58, m0
	s_mov_b32 m0, s36
	s_nop 2
	global_load_lds_dwordx4 v230, s[66:67]
	s_mov_b32 m0, s58
	s_waitcnt vmcnt(8)
	s_waitcnt lgkmcnt(0)
	s_barrier
	v_mfma_f32_16x16x32_bf16 v[62:65], v[130:133], v[162:165], v[62:65]
	v_mfma_f32_16x16x32_bf16 v[58:61], v[138:141], v[162:165], v[58:61]
	v_mfma_f32_16x16x32_bf16 v[54:57], v[130:133], v[170:173], v[54:57]
	v_mfma_f32_16x16x32_bf16 v[46:49], v[138:141], v[170:173], v[46:49]
	v_mfma_f32_16x16x32_bf16 v[38:41], v[130:133], v[178:181], v[38:41]
	v_mfma_f32_16x16x32_bf16 v[30:33], v[138:141], v[178:181], v[30:33]
	v_mfma_f32_16x16x32_bf16 v[22:25], v[130:133], v[186:189], v[22:25]
	v_mfma_f32_16x16x32_bf16 v[14:17], v[138:141], v[186:189], v[14:17]
	v_mfma_f32_16x16x32_bf16 v[62:65], v[134:137], v[166:169], v[62:65]
	v_mfma_f32_16x16x32_bf16 v[58:61], v[142:145], v[166:169], v[58:61]
	v_mfma_f32_16x16x32_bf16 v[54:57], v[134:137], v[174:177], v[54:57]
	v_mfma_f32_16x16x32_bf16 v[46:49], v[142:145], v[174:177], v[46:49]
	v_mfma_f32_16x16x32_bf16 v[38:41], v[134:137], v[182:185], v[38:41]
	v_mfma_f32_16x16x32_bf16 v[30:33], v[142:145], v[182:185], v[30:33]
	v_mfma_f32_16x16x32_bf16 v[22:25], v[134:137], v[190:193], v[22:25]
	v_mfma_f32_16x16x32_bf16 v[14:17], v[142:145], v[190:193], v[14:17]
	v_mfma_f32_16x16x32_bf16 v[50:53], v[146:149], v[162:165], v[50:53]
	v_mfma_f32_16x16x32_bf16 v[42:45], v[154:157], v[162:165], v[42:45]
	v_mfma_f32_16x16x32_bf16 v[34:37], v[146:149], v[170:173], v[34:37]
	v_mfma_f32_16x16x32_bf16 v[26:29], v[154:157], v[170:173], v[26:29]
	v_mfma_f32_16x16x32_bf16 v[18:21], v[146:149], v[178:181], v[18:21]
	v_mfma_f32_16x16x32_bf16 v[10:13], v[154:157], v[178:181], v[10:13]
	v_mfma_f32_16x16x32_bf16 v[6:9], v[146:149], v[186:189], v[6:9]
	v_mfma_f32_16x16x32_bf16 v[2:5], v[154:157], v[186:189], v[2:5]
	v_mfma_f32_16x16x32_bf16 v[50:53], v[150:153], v[166:169], v[50:53]
	v_mfma_f32_16x16x32_bf16 v[42:45], v[158:161], v[166:169], v[42:45]
	v_mfma_f32_16x16x32_bf16 v[34:37], v[150:153], v[174:177], v[34:37]
	v_mfma_f32_16x16x32_bf16 v[26:29], v[158:161], v[174:177], v[26:29]
	v_mfma_f32_16x16x32_bf16 v[18:21], v[150:153], v[182:185], v[18:21]
	v_mfma_f32_16x16x32_bf16 v[10:13], v[158:161], v[182:185], v[10:13]
	v_mfma_f32_16x16x32_bf16 v[6:9], v[150:153], v[190:193], v[6:9]
	v_mfma_f32_16x16x32_bf16 v[2:5], v[158:161], v[190:193], v[2:5]
	s_barrier
.Lmid1440:
	ds_read_b128 v[130:133], v237
	ds_read_b128 v[134:137], v237 offset:1024
	ds_read_b128 v[138:141], v237 offset:2048
	ds_read_b128 v[142:145], v237 offset:3072
	ds_read_b128 v[146:149], v238
	ds_read_b128 v[150:153], v238 offset:1024
	ds_read_b128 v[154:157], v238 offset:2048
	ds_read_b128 v[158:161], v238 offset:3072
	ds_read_b128 v[162:165], v236 offset:32768
	ds_read_b128 v[166:169], v236 offset:33792
	ds_read_b128 v[170:173], v236 offset:34816
	ds_read_b128 v[174:177], v236 offset:35840
	ds_read_b128 v[178:181], v236 offset:36864
	ds_read_b128 v[182:185], v236 offset:37888
	ds_read_b128 v[186:189], v236 offset:38912
	ds_read_b128 v[190:193], v236 offset:39936
	s_add_u32 s58, s66, 0x40000
	s_addc_u32 s59, s67, 0
	s_mov_b32 s66, m0
	s_mov_b32 m0, s37
	s_nop 2
	global_load_lds_dwordx4 v228, s[58:59]
	s_mov_b32 m0, s66
	s_nop 0
	s_mov_b32 s66, m0
	s_mov_b32 m0, s52
	s_nop 2
	global_load_lds_dwordx4 v230, s[58:59]
	s_mov_b32 m0, s66
	s_waitcnt vmcnt(8)
	s_waitcnt lgkmcnt(0)
	s_barrier
	v_mfma_f32_16x16x32_bf16 v[126:129], v[130:133], v[162:165], v[126:129]
	v_mfma_f32_16x16x32_bf16 v[122:125], v[138:141], v[162:165], v[122:125]
	v_mfma_f32_16x16x32_bf16 v[114:117], v[130:133], v[170:173], v[114:117]
	v_mfma_f32_16x16x32_bf16 v[106:109], v[138:141], v[170:173], v[106:109]
	v_mfma_f32_16x16x32_bf16 v[94:97], v[130:133], v[178:181], v[94:97]
	v_mfma_f32_16x16x32_bf16 v[90:93], v[138:141], v[178:181], v[90:93]
	v_mfma_f32_16x16x32_bf16 v[86:89], v[130:133], v[186:189], v[86:89]
	v_mfma_f32_16x16x32_bf16 v[78:81], v[138:141], v[186:189], v[78:81]
	v_mfma_f32_16x16x32_bf16 v[126:129], v[134:137], v[166:169], v[126:129]
	v_mfma_f32_16x16x32_bf16 v[122:125], v[142:145], v[166:169], v[122:125]
	v_mfma_f32_16x16x32_bf16 v[114:117], v[134:137], v[174:177], v[114:117]
	v_mfma_f32_16x16x32_bf16 v[106:109], v[142:145], v[174:177], v[106:109]
	v_mfma_f32_16x16x32_bf16 v[94:97], v[134:137], v[182:185], v[94:97]
	v_mfma_f32_16x16x32_bf16 v[90:93], v[142:145], v[182:185], v[90:93]
	v_mfma_f32_16x16x32_bf16 v[86:89], v[134:137], v[190:193], v[86:89]
	v_mfma_f32_16x16x32_bf16 v[78:81], v[142:145], v[190:193], v[78:81]
	v_mfma_f32_16x16x32_bf16 v[118:121], v[146:149], v[162:165], v[118:121]
	v_mfma_f32_16x16x32_bf16 v[110:113], v[154:157], v[162:165], v[110:113]
	v_mfma_f32_16x16x32_bf16 v[102:105], v[146:149], v[170:173], v[102:105]
	v_mfma_f32_16x16x32_bf16 v[98:101], v[154:157], v[170:173], v[98:101]
	v_mfma_f32_16x16x32_bf16 v[82:85], v[146:149], v[178:181], v[82:85]
	v_mfma_f32_16x16x32_bf16 v[74:77], v[154:157], v[178:181], v[74:77]
	v_mfma_f32_16x16x32_bf16 v[70:73], v[146:149], v[186:189], v[70:73]
	v_mfma_f32_16x16x32_bf16 v[66:69], v[154:157], v[186:189], v[66:69]
	v_mfma_f32_16x16x32_bf16 v[118:121], v[150:153], v[166:169], v[118:121]
	v_mfma_f32_16x16x32_bf16 v[110:113], v[158:161], v[166:169], v[110:113]
	v_mfma_f32_16x16x32_bf16 v[102:105], v[150:153], v[174:177], v[102:105]
	v_mfma_f32_16x16x32_bf16 v[98:101], v[158:161], v[174:177], v[98:101]
	v_mfma_f32_16x16x32_bf16 v[82:85], v[150:153], v[182:185], v[82:85]
	v_mfma_f32_16x16x32_bf16 v[74:77], v[158:161], v[182:185], v[74:77]
	v_mfma_f32_16x16x32_bf16 v[70:73], v[150:153], v[190:193], v[70:73]
	v_mfma_f32_16x16x32_bf16 v[66:69], v[158:161], v[190:193], v[66:69]
	s_barrier
	ds_read_b128 v[162:165], v236 offset:49152
	ds_read_b128 v[166:169], v236 offset:50176
	ds_read_b128 v[170:173], v236 offset:51200
	ds_read_b128 v[174:177], v236 offset:52224
	ds_read_b128 v[178:181], v236 offset:53248
	ds_read_b128 v[182:185], v236 offset:54272
	ds_read_b128 v[186:189], v236 offset:55296
	ds_read_b128 v[190:193], v236 offset:56320
	s_add_u32 s58, s64, 0x80
	s_addc_u32 s59, s65, 0
	s_mov_b32 s66, m0
	s_mov_b32 m0, s68
	s_nop 2
	global_load_lds_dwordx4 v229, s[58:59]
	s_mov_b32 m0, s66
	s_nop 0
	s_mov_b32 s66, m0
	s_mov_b32 m0, s69
	s_nop 2
	global_load_lds_dwordx4 v231, s[58:59]
	s_mov_b32 m0, s66
	s_add_u32 s58, s64, 0x40080
	s_addc_u32 s59, s65, 0
	s_mov_b32 s64, m0
	s_mov_b32 m0, s78
	s_nop 2
	global_load_lds_dwordx4 v229, s[58:59]
	s_mov_b32 m0, s64
	s_nop 0
	s_mov_b32 s64, m0
	s_mov_b32 m0, s79
	s_nop 2
	global_load_lds_dwordx4 v231, s[58:59]
	s_mov_b32 m0, s64
	s_mov_b32 s58, m0
	s_mov_b32 m0, s76
	s_nop 2
	global_load_lds_dwordx4 v228, s[62:63]
	s_mov_b32 m0, s58
	s_nop 0
	s_mov_b32 s58, m0
	s_mov_b32 m0, s77
	s_nop 2
	global_load_lds_dwordx4 v230, s[62:63]
	s_mov_b32 m0, s58
	s_waitcnt vmcnt(8)
	s_waitcnt lgkmcnt(0)
	s_barrier
	v_mfma_f32_16x16x32_bf16 v[62:65], v[130:133], v[162:165], v[62:65]
	v_mfma_f32_16x16x32_bf16 v[58:61], v[138:141], v[162:165], v[58:61]
	v_mfma_f32_16x16x32_bf16 v[54:57], v[130:133], v[170:173], v[54:57]
	v_mfma_f32_16x16x32_bf16 v[46:49], v[138:141], v[170:173], v[46:49]
	v_mfma_f32_16x16x32_bf16 v[38:41], v[130:133], v[178:181], v[38:41]
	v_mfma_f32_16x16x32_bf16 v[30:33], v[138:141], v[178:181], v[30:33]
	v_mfma_f32_16x16x32_bf16 v[22:25], v[130:133], v[186:189], v[22:25]
	v_mfma_f32_16x16x32_bf16 v[14:17], v[138:141], v[186:189], v[14:17]
	v_mfma_f32_16x16x32_bf16 v[62:65], v[134:137], v[166:169], v[62:65]
	v_mfma_f32_16x16x32_bf16 v[58:61], v[142:145], v[166:169], v[58:61]
	v_mfma_f32_16x16x32_bf16 v[54:57], v[134:137], v[174:177], v[54:57]
	v_mfma_f32_16x16x32_bf16 v[46:49], v[142:145], v[174:177], v[46:49]
	v_mfma_f32_16x16x32_bf16 v[38:41], v[134:137], v[182:185], v[38:41]
	v_mfma_f32_16x16x32_bf16 v[30:33], v[142:145], v[182:185], v[30:33]
	v_mfma_f32_16x16x32_bf16 v[22:25], v[134:137], v[190:193], v[22:25]
	v_mfma_f32_16x16x32_bf16 v[14:17], v[142:145], v[190:193], v[14:17]
	v_mfma_f32_16x16x32_bf16 v[50:53], v[146:149], v[162:165], v[50:53]
	v_mfma_f32_16x16x32_bf16 v[42:45], v[154:157], v[162:165], v[42:45]
	v_mfma_f32_16x16x32_bf16 v[34:37], v[146:149], v[170:173], v[34:37]
	v_mfma_f32_16x16x32_bf16 v[26:29], v[154:157], v[170:173], v[26:29]
	v_mfma_f32_16x16x32_bf16 v[18:21], v[146:149], v[178:181], v[18:21]
	v_mfma_f32_16x16x32_bf16 v[10:13], v[154:157], v[178:181], v[10:13]
	v_mfma_f32_16x16x32_bf16 v[6:9], v[146:149], v[186:189], v[6:9]
	v_mfma_f32_16x16x32_bf16 v[2:5], v[154:157], v[186:189], v[2:5]
	v_mfma_f32_16x16x32_bf16 v[50:53], v[150:153], v[166:169], v[50:53]
	v_mfma_f32_16x16x32_bf16 v[42:45], v[158:161], v[166:169], v[42:45]
	v_mfma_f32_16x16x32_bf16 v[34:37], v[150:153], v[174:177], v[34:37]
	v_mfma_f32_16x16x32_bf16 v[26:29], v[158:161], v[174:177], v[26:29]
	v_mfma_f32_16x16x32_bf16 v[18:21], v[150:153], v[182:185], v[18:21]
	v_mfma_f32_16x16x32_bf16 v[10:13], v[158:161], v[182:185], v[10:13]
	v_mfma_f32_16x16x32_bf16 v[6:9], v[150:153], v[190:193], v[6:9]
	v_mfma_f32_16x16x32_bf16 v[2:5], v[158:161], v[190:193], v[2:5]
	s_barrier
	s_add_i32 s87, s87, 2
	s_add_u32 s85, s85, 0x100
	s_addc_u32 s86, s86, 0
	s_cmp_gt_u32 s87, 13
	s_mov_b64 s[58:59], s[60:61]
	s_cbranch_scc0 .LBB0_1440
	s_and_b64 vcc, exec, s[16:17]
	s_cbranch_vccz .LBB0_1443
	s_barrier
